# P5 mid-K rescale: sixteen g_a/g_b quads kept in flight in the dead fragment registers behind counted waits
# speedup vs baseline: 1.0056x; 1.0035x over previous
; __device__ __forceinline__ void unpack8(u32x4 w, f32x4& a, f32x4& b) { a = (f32x4){bflo(w.x), bfhi(w.x), bflo(w.y), bfhi(w.y)}; b = (f32x4){bflo(w.z), bfhi(w.z), bflo(w.w), bfhi(w.w)}; }
;     __device__ __forceinline__ void mid(Acc& acc, const Unit& u, int wr, int wc, int fr, int fq) const {
;         const int row0 = u.row0 + wr * 64 + fr, col0 = u.col0 + wc * 32 + 8 * fq;
; #pragma unroll
;         for (int ai = 0; ai < 2; ++ai)
; #pragma unroll
;             for (int m = 0; m < 4; ++m) { const size_t ro = (size_t)(row0 + ai * HALF + m * 16) * ldg;
; #pragma unroll
;                 for (int bj = 0; bj < 2; ++bj) { const int col = col0 + bj * HALF;
;                     f32x4 a0, a1, b0, b1; unpack8(*(const u32x4*)(GA + ro + col), a0, a1); unpack8(*(const u32x4*)(GB + ro + col), b0, b1);
; #pragma unroll
;                     for (int j = 0; j < 4; ++j) { acc[ai][bj][m][0][j] *= (1.0f + __expf(-b0[j])) * __builtin_amdgcn_rcpf(1.0f + __expf(-a0[j])); acc[ai][bj][m][1][j] *= (1.0f + __expf(-b1[j])) * __builtin_amdgcn_rcpf(1.0f + __expf(-a1[j])); } } }
; template <class Epi, class Sched, bool F8 = false, bool MID = false, bool GATHER = false>
; __device__ __forceinline__ void gemm_phase(LAS unsigned char* lds, const Gemm g, const Sched& S, const Epi& E) {
;     ...
;             if constexpr (MID) { if (t == (nt >> 1)) { if constexpr (F8) asm volatile("s_nop 15\n\ts_nop 15" ::: "memory"); int l_; asm volatile("v_mbcnt_lo_u32_b32 %0, -1, 0\n\tv_mbcnt_hi_u32_b32 %0, -1, %0" : "=v"(l_)); E.mid(acc, cur, wr, wc, l_ & 15, l_ >> 4); if constexpr (F8) asm volatile("s_nop 7" ::: "memory"); } }
.LBB0_1851:
	s_cmp_lg_u32 s86, 6
	s_cbranch_scc1 .LBB0_1850
	v_mbcnt_lo_u32_b32 v250, -1, 0
	v_mbcnt_hi_u32_b32 v250, -1, v250
	v_and_b32_e32 v251, 15, v250
	v_add_u32_e32 v251, s78, v251
	v_mul_lo_u32 v251, v251, s73
	v_ashrrev_i32_e32 v250, 1, v250
	v_and_b32_e32 v250, -8, v250
	v_add_u32_e32 v250, s77, v250
	v_lshl_add_u32 v250, v250, 1, v251
	v_mov_b32_e32 v251, v250
	global_load_dwordx4 v[182:185], v251, s[6:7]
	global_load_dwordx4 v[186:189], v251, s[8:9]
	global_load_dwordx4 v[190:193], v251, s[6:7] offset:256
	global_load_dwordx4 v[194:197], v251, s[8:9] offset:256
	s_mul_i32 s98, s73, 0x10
	v_add_u32_e32 v251, s98, v250
	global_load_dwordx4 v[198:201], v251, s[6:7]
	global_load_dwordx4 v[202:205], v251, s[8:9]
	global_load_dwordx4 v[206:209], v251, s[6:7] offset:256
	global_load_dwordx4 v[210:213], v251, s[8:9] offset:256
	s_mul_i32 s98, s73, 0x20
	v_add_u32_e32 v251, s98, v250
	global_load_dwordx4 v[214:217], v251, s[6:7]
	global_load_dwordx4 v[218:221], v251, s[8:9]
	global_load_dwordx4 v[222:225], v251, s[6:7] offset:256
	global_load_dwordx4 v[226:229], v251, s[8:9] offset:256
	s_mul_i32 s98, s73, 0x30
	v_add_u32_e32 v251, s98, v250
	global_load_dwordx4 v[230:233], v251, s[6:7]
	global_load_dwordx4 v[234:237], v251, s[8:9]
	global_load_dwordx4 v[238:241], v251, s[6:7] offset:256
	global_load_dwordx4 v[242:245], v251, s[8:9] offset:256
	s_nop 15
	s_nop 15
	v_mbcnt_lo_u32_b32 v2, -1, 0
	v_mbcnt_hi_u32_b32 v2, -1, v2
	v_mov_b64_e32 v[4:5], s[6:7]
	v_and_b32_e32 v3, 15, v2
	v_ashrrev_i32_e32 v2, 1, v2
	v_and_b32_e32 v2, -8, v2
	v_add_u32_e32 v2, s77, v2
	v_add_u32_e32 v8, s78, v3
	v_ashrrev_i32_e32 v3, 31, v2
	v_mad_i64_i32 v[6:7], s[26:27], v8, s73, v[4:5]
	v_lshlrev_b64 v[2:3], 1, v[2:3]
	v_lshl_add_u64 v[12:13], v[6:7], 0, v[2:3]
	v_mov_b64_e32 v[6:7], s[8:9]
	v_mad_i64_i32 v[156:157], s[26:27], v8, s73, v[6:7]
	v_lshl_add_u64 v[168:169], v[156:157], 0, v[2:3]
	v_add_u32_e32 v9, 16, v8
	s_waitcnt vmcnt(15)
	v_mov_b32_e32 v152, v182
	v_mov_b32_e32 v153, v183
	v_mov_b32_e32 v154, v184
	v_mov_b32_e32 v155, v185
	s_mul_i32 s98, s73, 0x80
	v_add_u32_e32 v251, s98, v250
	global_load_dwordx4 v[182:185], v251, s[6:7]
	v_lshlrev_b32_e32 v11, 16, v152
	v_and_b32_e32 v12, 0xffff0000, v152
	s_waitcnt vmcnt(15)
	v_mov_b32_e32 v156, v186
	v_mov_b32_e32 v157, v187
	v_mov_b32_e32 v158, v188
	v_mov_b32_e32 v159, v189
	s_mul_i32 s98, s73, 0x80
	v_add_u32_e32 v251, s98, v250
	global_load_dwordx4 v[186:189], v251, s[8:9]
	v_lshlrev_b32_e32 v165, 16, v156
	v_lshlrev_b32_e32 v172, 16, v158
	v_lshlrev_b32_e32 v13, 16, v153
	v_and_b32_e32 v151, 0xffff0000, v153
	v_lshlrev_b32_e32 v152, 16, v154
	v_and_b32_e32 v153, 0xffff0000, v154
	v_lshlrev_b32_e32 v154, 16, v155
	v_and_b32_e32 v155, 0xffff0000, v155
	v_lshlrev_b32_e32 v167, 16, v157
	v_and_b32_e32 v157, 0xffff0000, v157
	v_and_b32_e32 v158, 0xffff0000, v158
	v_lshlrev_b32_e32 v173, 16, v159
	v_and_b32_e32 v159, 0xffff0000, v159
	s_waitcnt vmcnt(15)
	v_mov_b32_e32 v160, v190
	v_mov_b32_e32 v161, v191
	v_mov_b32_e32 v162, v192
	v_mov_b32_e32 v163, v193
	s_mul_i32 s98, s73, 0x80
	v_add_u32_e32 v251, s98, v250
	global_load_dwordx4 v[190:193], v251, s[6:7] offset:256
	v_lshlrev_b32_e32 v178, 16, v160
	v_and_b32_e32 v179, 0xffff0000, v160
	v_mul_f32_e32 v160, 0xbfb8aa3b, v165
	v_mul_f32_e32 v11, 0xbfb8aa3b, v11
	v_mul_f32_e32 v165, 0xbfb8aa3b, v172
	v_mul_f32_e32 v174, 0xbfb8aa3b, v12
	v_mul_f32_e32 v172, 0xbfb8aa3b, v152
	v_mul_f32_e32 v158, 0xbfb8aa3b, v158
	v_mul_f32_e32 v175, 0xbfb8aa3b, v153
	v_mul_f32_e32 v157, 0xbfb8aa3b, v157
	v_mul_f32_e32 v159, 0xbfb8aa3b, v159
	v_mul_f32_e32 v180, 0xbfb8aa3b, v155
	v_exp_f32_e32 v11, v11
	v_exp_f32_e32 v152, v165
	v_exp_f32_e32 v165, v174
	v_mul_f32_e32 v167, 0xbfb8aa3b, v167
	v_mul_f32_e32 v176, 0xbfb8aa3b, v13
	v_mul_f32_e32 v151, 0xbfb8aa3b, v151
	v_exp_f32_e32 v153, v158
	v_exp_f32_e32 v158, v175
	v_exp_f32_e32 v155, v157
	v_exp_f32_e32 v157, v159
	v_exp_f32_e32 v159, v180
	v_and_b32_e32 v156, 0xffff0000, v156
	v_mul_f32_e32 v177, 0xbfb8aa3b, v154
	v_exp_f32_e32 v12, v160
	v_exp_f32_e32 v160, v172
	v_exp_f32_e32 v154, v167
	v_exp_f32_e32 v167, v176
	v_exp_f32_e32 v151, v151
	v_mul_f32_e32 v156, 0xbfb8aa3b, v156
	v_exp_f32_e32 v172, v177
	v_mul_f32_e32 v173, 0xbfb8aa3b, v173
	v_exp_f32_e32 v13, v156
	v_add_f32_e32 v11, 1.0, v11
	v_add_f32_e32 v165, 1.0, v165
	v_exp_f32_e32 v156, v173
	v_add_f32_e32 v173, 1.0, v158
	v_add_f32_e32 v177, 1.0, v159
	v_rcp_f32_e32 v158, v11
	v_rcp_f32_e32 v159, v165
	v_add_f32_e32 v160, 1.0, v160
	v_add_f32_e32 v167, 1.0, v167
	v_add_f32_e32 v151, 1.0, v151
	v_add_f32_e32 v176, 1.0, v172
	v_rcp_f32_e32 v172, v160
	v_rcp_f32_e32 v173, v173
	v_rcp_f32_e32 v174, v167
	v_rcp_f32_e32 v175, v151
	v_pk_add_f32 v[12:13], v[12:13], 1.0 op_sel_hi:[1,0]
	v_pk_add_f32 v[154:155], v[154:155], 1.0 op_sel_hi:[1,0]
	v_pk_mul_f32 v[12:13], v[158:159], v[12:13]
	v_pk_add_f32 v[152:153], v[152:153], 1.0 op_sel_hi:[1,0]
	v_pk_mul_f32 v[138:139], v[138:139], v[12:13]
	v_mad_i64_i32 v[12:13], s[26:27], v9, s73, v[4:5]
	v_pk_mul_f32 v[154:155], v[174:175], v[154:155]
	v_pk_mul_f32 v[152:153], v[172:173], v[152:153]
	v_lshl_add_u64 v[12:13], v[12:13], 0, v[2:3]
	v_rcp_f32_e32 v176, v176
	v_rcp_f32_e32 v177, v177
	v_pk_mul_f32 v[140:141], v[140:141], v[154:155]
	v_pk_mul_f32 v[134:135], v[134:135], v[152:153]
	v_pk_add_f32 v[156:157], v[156:157], 1.0 op_sel_hi:[1,0]
	v_lshlrev_b32_e32 v11, 16, v161
	v_pk_mul_f32 v[156:157], v[176:177], v[156:157]
	v_and_b32_e32 v151, 0xffff0000, v161
	v_pk_mul_f32 v[136:137], v[136:137], v[156:157]
	v_mad_i64_i32 v[156:157], s[26:27], v9, s73, v[6:7]
	v_lshl_add_u64 v[172:173], v[156:157], 0, v[2:3]
	v_lshlrev_b32_e32 v161, 16, v162
	v_and_b32_e32 v165, 0xffff0000, v162
	v_mul_f32_e32 v161, 0xbfb8aa3b, v161
	v_mul_f32_e32 v165, 0xbfb8aa3b, v165
	v_lshlrev_b32_e32 v167, 16, v163
	v_and_b32_e32 v9, 0xffff0000, v163
	s_waitcnt vmcnt(15)
; __device__ __forceinline__ void unpack8(u32x4 w, f32x4& a, f32x4& b) { a = (f32x4){bflo(w.x), bfhi(w.x), bflo(w.y), bfhi(w.y)}; b = (f32x4){bflo(w.z), bfhi(w.z), bflo(w.w), bfhi(w.w)}; }
;     __device__ __forceinline__ void mid(Acc& acc, const Unit& u, int wr, int wc, int fr, int fq) const {
;         const int row0 = u.row0 + wr * 64 + fr, col0 = u.col0 + wc * 32 + 8 * fq;
; #pragma unroll
;         for (int ai = 0; ai < 2; ++ai)
; #pragma unroll
;             for (int m = 0; m < 4; ++m) { const size_t ro = (size_t)(row0 + ai * HALF + m * 16) * ldg;
; #pragma unroll
;                 for (int bj = 0; bj < 2; ++bj) { const int col = col0 + bj * HALF;
;                     f32x4 a0, a1, b0, b1; unpack8(*(const u32x4*)(GA + ro + col), a0, a1); unpack8(*(const u32x4*)(GB + ro + col), b0, b1);
; #pragma unroll
;                     for (int j = 0; j < 4; ++j) { acc[ai][bj][m][0][j] *= (1.0f + __expf(-b0[j])) * __builtin_amdgcn_rcpf(1.0f + __expf(-a0[j])); acc[ai][bj][m][1][j] *= (1.0f + __expf(-b1[j])) * __builtin_amdgcn_rcpf(1.0f + __expf(-a1[j])); } } }
; template <class Epi, class Sched, bool F8 = false, bool MID = false, bool GATHER = false>
; __device__ __forceinline__ void gemm_phase(LAS unsigned char* lds, const Gemm g, const Sched& S, const Epi& E) {
;     ...
;             if constexpr (MID) { if (t == (nt >> 1)) { if constexpr (F8) asm volatile("s_nop 15\n\ts_nop 15" ::: "memory"); int l_; asm volatile("v_mbcnt_lo_u32_b32 %0, -1, 0\n\tv_mbcnt_hi_u32_b32 %0, -1, %0" : "=v"(l_)); E.mid(acc, cur, wr, wc, l_ & 15, l_ >> 4); if constexpr (F8) asm volatile("s_nop 7" ::: "memory"); } }
	v_mov_b32_e32 v168, v194
	v_mov_b32_e32 v169, v195
	v_mov_b32_e32 v170, v196
	v_mov_b32_e32 v171, v197
	s_mul_i32 s98, s73, 0x80
	v_add_u32_e32 v251, s98, v250
	global_load_dwordx4 v[194:197], v251, s[8:9] offset:256
	v_lshlrev_b32_e32 v160, 16, v168
	v_and_b32_e32 v163, 0xffff0000, v168
	v_lshlrev_b32_e32 v174, 16, v169
	v_and_b32_e32 v175, 0xffff0000, v169
	v_lshlrev_b32_e32 v168, 16, v170
	v_and_b32_e32 v169, 0xffff0000, v170
	v_exp_f32_e32 v161, v161
	v_mul_f32_e32 v170, 0xbfb8aa3b, v179
	v_exp_f32_e32 v165, v165
	v_lshlrev_b32_e32 v177, 16, v171
	v_and_b32_e32 v181, 0xffff0000, v171
	v_exp_f32_e32 v171, v170
	v_add_f32_e32 v161, 1.0, v161
	v_add_f32_e32 v165, 1.0, v165
	v_mul_f32_e32 v11, 0xbfb8aa3b, v11
	v_rcp_f32_e32 v170, v161
	v_mul_f32_e32 v161, 0xbfb8aa3b, v163
	v_add_f32_e32 v163, 1.0, v171
	v_exp_f32_e32 v11, v11
	v_rcp_f32_e32 v171, v165
	v_mul_f32_e32 v165, 0xbfb8aa3b, v174
	v_exp_f32_e32 v174, v165
	v_mul_f32_e32 v165, 0xbfb8aa3b, v167
	v_mul_f32_e32 v162, 0xbfb8aa3b, v178
	v_exp_f32_e32 v165, v165
	v_mul_f32_e32 v151, 0xbfb8aa3b, v151
	v_exp_f32_e32 v162, v162
	v_exp_f32_e32 v151, v151
	v_add_f32_e32 v11, 1.0, v11
	v_mul_f32_e32 v9, 0xbfb8aa3b, v9
	v_rcp_f32_e32 v176, v11
	v_mul_f32_e32 v11, 0xbfb8aa3b, v177
	v_exp_f32_e32 v9, v9
	v_mul_f32_e32 v160, 0xbfb8aa3b, v160
	v_exp_f32_e32 v178, v11
	v_add_f32_e32 v11, 1.0, v165
	v_mul_f32_e32 v165, 0xbfb8aa3b, v175
	v_exp_f32_e32 v160, v160
	v_add_f32_e32 v162, 1.0, v162
	v_exp_f32_e32 v161, v161
	v_exp_f32_e32 v175, v165
	v_rcp_f32_e32 v180, v11
	v_add_f32_e32 v11, 1.0, v151
	v_rcp_f32_e32 v162, v162
	v_mul_f32_e32 v168, 0xbfb8aa3b, v168
	v_rcp_f32_e32 v163, v163
	v_mul_f32_e32 v169, 0xbfb8aa3b, v169
	v_rcp_f32_e32 v177, v11
	v_mul_f32_e32 v11, 0xbfb8aa3b, v181
	v_exp_f32_e32 v168, v168
	v_exp_f32_e32 v169, v169
	v_exp_f32_e32 v179, v11
	v_add_f32_e32 v9, 1.0, v9
	v_rcp_f32_e32 v181, v9
	v_pk_add_f32 v[174:175], v[174:175], 1.0 op_sel_hi:[1,0]
	v_pk_add_f32 v[160:161], v[160:161], 1.0 op_sel_hi:[1,0]
	s_nop 0
	v_pk_mul_f32 v[160:161], v[160:161], v[162:163]
	v_pk_mul_f32 v[162:163], v[174:175], v[176:177]
	v_pk_mul_f32 v[130:131], v[130:131], v[160:161]
	v_pk_mul_f32 v[132:133], v[132:133], v[162:163]
	v_pk_add_f32 v[160:161], v[178:179], 1.0 op_sel_hi:[1,0]
	v_pk_add_f32 v[162:163], v[168:169], 1.0 op_sel_hi:[1,0]
	s_waitcnt vmcnt(15)
	v_mov_b32_e32 v152, v198
	v_mov_b32_e32 v153, v199
	v_mov_b32_e32 v154, v200
	v_mov_b32_e32 v155, v201
	s_mul_i32 s98, s73, 0x90
	v_add_u32_e32 v251, s98, v250
	global_load_dwordx4 v[198:201], v251, s[6:7]
	s_waitcnt vmcnt(15)
	v_mov_b32_e32 v156, v202
	v_mov_b32_e32 v157, v203
	v_mov_b32_e32 v158, v204
	v_mov_b32_e32 v159, v205
	s_mul_i32 s98, s73, 0x90
	v_add_u32_e32 v251, s98, v250
	global_load_dwordx4 v[202:205], v251, s[8:9]
	v_lshlrev_b32_e32 v174, 16, v159
	v_pk_mul_f32 v[168:169], v[162:163], v[170:171]
	v_pk_mul_f32 v[170:171], v[160:161], v[180:181]
	v_pk_mul_f32 v[128:129], v[128:129], v[170:171]
	v_lshlrev_b32_e32 v9, 16, v152
	v_and_b32_e32 v11, 0xffff0000, v152
	v_lshlrev_b32_e32 v151, 16, v153
	v_and_b32_e32 v165, 0xffff0000, v153
	v_lshlrev_b32_e32 v13, 16, v154
	v_and_b32_e32 v167, 0xffff0000, v154
	v_lshlrev_b32_e32 v171, 16, v155
	v_and_b32_e32 v175, 0xffff0000, v155
	v_mul_f32_e32 v9, 0xbfb8aa3b, v9
	v_exp_f32_e32 v9, v9
	v_mul_f32_e32 v13, 0xbfb8aa3b, v13
	v_exp_f32_e32 v13, v13
	v_mul_f32_e32 v11, 0xbfb8aa3b, v11
	v_lshlrev_b32_e32 v170, 16, v157
	v_and_b32_e32 v173, 0xffff0000, v157
	v_lshlrev_b32_e32 v157, 16, v158
	v_add_f32_e32 v9, 1.0, v9
	v_exp_f32_e32 v11, v11
	v_pk_mul_f32 v[126:127], v[126:127], v[168:169]
	v_lshlrev_b32_e32 v12, 16, v156
	v_and_b32_e32 v169, 0xffff0000, v156
	v_rcp_f32_e32 v156, v9
	v_mul_f32_e32 v9, 0xbfb8aa3b, v157
	v_and_b32_e32 v172, 0xffff0000, v158
	v_exp_f32_e32 v158, v9
	v_add_f32_e32 v9, 1.0, v13
	v_rcp_f32_e32 v168, v9
	v_mul_f32_e32 v9, 0xbfb8aa3b, v169
	v_exp_f32_e32 v13, v9
	v_add_f32_e32 v9, 1.0, v11
	v_mul_f32_e32 v11, 0xbfb8aa3b, v167
	v_exp_f32_e32 v11, v11
	v_rcp_f32_e32 v157, v9
	v_mul_f32_e32 v9, 0xbfb8aa3b, v172
	v_and_b32_e32 v177, 0xffff0000, v159
	v_exp_f32_e32 v159, v9
	v_add_f32_e32 v9, 1.0, v11
	v_mul_f32_e32 v11, 0xbfb8aa3b, v151
	v_exp_f32_e32 v11, v11
	v_rcp_f32_e32 v169, v9
	v_mul_f32_e32 v9, 0xbfb8aa3b, v170
	v_exp_f32_e32 v170, v9
	v_add_f32_e32 v9, 1.0, v11
	v_mul_f32_e32 v11, 0xbfb8aa3b, v171
	v_exp_f32_e32 v11, v11
	v_rcp_f32_e32 v172, v9
	v_mul_f32_e32 v9, 0xbfb8aa3b, v174
	v_exp_f32_e32 v174, v9
	v_add_f32_e32 v9, 1.0, v11
	v_mul_f32_e32 v11, 0xbfb8aa3b, v165
	v_exp_f32_e32 v11, v11
	v_rcp_f32_e32 v176, v9
	v_mul_f32_e32 v151, 0xbfb8aa3b, v173
	v_mul_f32_e32 v12, 0xbfb8aa3b, v12
	v_add_f32_e32 v9, 1.0, v11
	v_rcp_f32_e32 v173, v9
	v_mul_f32_e32 v9, 0xbfb8aa3b, v175
	v_exp_f32_e32 v9, v9
	v_exp_f32_e32 v12, v12
	v_mul_f32_e32 v11, 0xbfb8aa3b, v177
	v_exp_f32_e32 v171, v151
	v_exp_f32_e32 v175, v11
	v_add_f32_e32 v9, 1.0, v9
	v_rcp_f32_e32 v177, v9
	v_pk_add_f32 v[12:13], v[12:13], 1.0 op_sel_hi:[1,0]
	v_pk_add_f32 v[170:171], v[170:171], 1.0 op_sel_hi:[1,0]
	v_pk_mul_f32 v[12:13], v[12:13], v[156:157]
	v_pk_mul_f32 v[156:157], v[170:171], v[172:173]
	v_pk_mul_f32 v[122:123], v[122:123], v[12:13]
	v_pk_add_f32 v[12:13], v[174:175], 1.0 op_sel_hi:[1,0]
	v_add_u32_e32 v151, 32, v8
	v_pk_mul_f32 v[12:13], v[12:13], v[176:177]
	v_pk_mul_f32 v[124:125], v[124:125], v[156:157]
	v_pk_add_f32 v[156:157], v[158:159], 1.0 op_sel_hi:[1,0]
	v_pk_mul_f32 v[120:121], v[120:121], v[12:13]
	v_mad_i64_i32 v[12:13], s[26:27], v151, s73, v[4:5]
	v_pk_mul_f32 v[156:157], v[156:157], v[168:169]
	v_lshl_add_u64 v[12:13], v[12:13], 0, v[2:3]
	v_pk_mul_f32 v[118:119], v[118:119], v[156:157]
	s_waitcnt vmcnt(15)
; __device__ __forceinline__ void unpack8(u32x4 w, f32x4& a, f32x4& b) { a = (f32x4){bflo(w.x), bfhi(w.x), bflo(w.y), bfhi(w.y)}; b = (f32x4){bflo(w.z), bfhi(w.z), bflo(w.w), bfhi(w.w)}; }
;     __device__ __forceinline__ void mid(Acc& acc, const Unit& u, int wr, int wc, int fr, int fq) const {
;         const int row0 = u.row0 + wr * 64 + fr, col0 = u.col0 + wc * 32 + 8 * fq;
; #pragma unroll
;         for (int ai = 0; ai < 2; ++ai)
; #pragma unroll
;             for (int m = 0; m < 4; ++m) { const size_t ro = (size_t)(row0 + ai * HALF + m * 16) * ldg;
; #pragma unroll
;                 for (int bj = 0; bj < 2; ++bj) { const int col = col0 + bj * HALF;
;                     f32x4 a0, a1, b0, b1; unpack8(*(const u32x4*)(GA + ro + col), a0, a1); unpack8(*(const u32x4*)(GB + ro + col), b0, b1);
; #pragma unroll
;                     for (int j = 0; j < 4; ++j) { acc[ai][bj][m][0][j] *= (1.0f + __expf(-b0[j])) * __builtin_amdgcn_rcpf(1.0f + __expf(-a0[j])); acc[ai][bj][m][1][j] *= (1.0f + __expf(-b1[j])) * __builtin_amdgcn_rcpf(1.0f + __expf(-a1[j])); } } }
; template <class Epi, class Sched, bool F8 = false, bool MID = false, bool GATHER = false>
; __device__ __forceinline__ void gemm_phase(LAS unsigned char* lds, const Gemm g, const Sched& S, const Epi& E) {
;     ...
;             if constexpr (MID) { if (t == (nt >> 1)) { if constexpr (F8) asm volatile("s_nop 15\n\ts_nop 15" ::: "memory"); int l_; asm volatile("v_mbcnt_lo_u32_b32 %0, -1, 0\n\tv_mbcnt_hi_u32_b32 %0, -1, %0" : "=v"(l_)); E.mid(acc, cur, wr, wc, l_ & 15, l_ >> 4); if constexpr (F8) asm volatile("s_nop 7" ::: "memory"); } }
	v_mov_b32_e32 v160, v206
	v_mov_b32_e32 v161, v207
	v_mov_b32_e32 v162, v208
	v_mov_b32_e32 v163, v209
	s_mul_i32 s98, s73, 0x90
	v_add_u32_e32 v251, s98, v250
	global_load_dwordx4 v[206:209], v251, s[6:7] offset:256
	v_lshlrev_b32_e32 v9, 16, v160
	v_and_b32_e32 v11, 0xffff0000, v160
	v_lshlrev_b32_e32 v165, 16, v161
	v_and_b32_e32 v167, 0xffff0000, v161
	v_mad_i64_i32 v[160:161], s[26:27], v151, s73, v[6:7]
	v_lshl_add_u64 v[160:161], v[160:161], 0, v[2:3]
	v_mul_f32_e32 v9, 0xbfb8aa3b, v9
	v_lshlrev_b32_e32 v172, 16, v162
	v_exp_f32_e32 v9, v9
	s_waitcnt vmcnt(15)
	v_mov_b32_e32 v152, v210
	v_mov_b32_e32 v153, v211
	v_mov_b32_e32 v154, v212
	v_mov_b32_e32 v155, v213
	s_mul_i32 s98, s73, 0x90
	v_add_u32_e32 v251, s98, v250
	global_load_dwordx4 v[210:213], v251, s[8:9] offset:256
	v_lshlrev_b32_e32 v174, 16, v153
	v_and_b32_e32 v177, 0xffff0000, v153
	v_lshlrev_b32_e32 v153, 16, v154
	v_and_b32_e32 v176, 0xffff0000, v154
	v_mul_f32_e32 v154, 0xbfb8aa3b, v172
	v_lshlrev_b32_e32 v178, 16, v155
	v_and_b32_e32 v179, 0xffff0000, v155
	v_exp_f32_e32 v155, v154
	v_mul_f32_e32 v11, 0xbfb8aa3b, v11
	v_add_f32_e32 v9, 1.0, v9
	v_exp_f32_e32 v11, v11
	v_and_b32_e32 v173, 0xffff0000, v162
	v_lshlrev_b32_e32 v162, 16, v152
	v_rcp_f32_e32 v154, v9
	v_mul_f32_e32 v9, 0xbfb8aa3b, v153
	v_lshlrev_b32_e32 v175, 16, v163
	v_and_b32_e32 v151, 0xffff0000, v163
	v_and_b32_e32 v163, 0xffff0000, v152
	v_mul_f32_e32 v152, 0xbfb8aa3b, v162
	v_exp_f32_e32 v162, v9
	v_add_f32_e32 v9, 1.0, v155
	v_rcp_f32_e32 v172, v9
	v_mul_f32_e32 v9, 0xbfb8aa3b, v163
	v_exp_f32_e32 v153, v9
	v_add_f32_e32 v9, 1.0, v11
	v_mul_f32_e32 v11, 0xbfb8aa3b, v173
	v_exp_f32_e32 v11, v11
	v_rcp_f32_e32 v155, v9
	v_mul_f32_e32 v9, 0xbfb8aa3b, v176
	v_exp_f32_e32 v163, v9
	v_add_f32_e32 v9, 1.0, v11
	v_mul_f32_e32 v11, 0xbfb8aa3b, v165
	v_exp_f32_e32 v11, v11
	v_rcp_f32_e32 v173, v9
	v_mul_f32_e32 v9, 0xbfb8aa3b, v174
	v_exp_f32_e32 v174, v9
	v_add_f32_e32 v9, 1.0, v11
	v_mul_f32_e32 v11, 0xbfb8aa3b, v175
	v_exp_f32_e32 v11, v11
	v_rcp_f32_e32 v176, v9
	v_mul_f32_e32 v9, 0xbfb8aa3b, v178
	v_exp_f32_e32 v178, v9
	v_add_f32_e32 v9, 1.0, v11
	v_mul_f32_e32 v11, 0xbfb8aa3b, v167
	v_exp_f32_e32 v11, v11
	v_rcp_f32_e32 v180, v9
	v_mul_f32_e32 v165, 0xbfb8aa3b, v177
	v_exp_f32_e32 v152, v152
	v_add_f32_e32 v9, 1.0, v11
	v_rcp_f32_e32 v177, v9
	v_mul_f32_e32 v9, 0xbfb8aa3b, v151
	v_exp_f32_e32 v9, v9
	v_exp_f32_e32 v175, v165
	v_mul_f32_e32 v11, 0xbfb8aa3b, v179
	v_exp_f32_e32 v179, v11
	v_add_f32_e32 v9, 1.0, v9
	v_rcp_f32_e32 v181, v9
	v_pk_add_f32 v[174:175], v[174:175], 1.0 op_sel_hi:[1,0]
	v_pk_add_f32 v[152:153], v[152:153], 1.0 op_sel_hi:[1,0]
	s_nop 0
	v_pk_mul_f32 v[152:153], v[152:153], v[154:155]
	v_pk_mul_f32 v[154:155], v[174:175], v[176:177]
	v_pk_mul_f32 v[114:115], v[114:115], v[152:153]
	v_pk_mul_f32 v[116:117], v[116:117], v[154:155]
	v_pk_add_f32 v[152:153], v[178:179], 1.0 op_sel_hi:[1,0]
	v_pk_add_f32 v[154:155], v[162:163], 1.0 op_sel_hi:[1,0]
	s_nop 0
	v_pk_mul_f32 v[162:163], v[154:155], v[172:173]
	v_pk_mul_f32 v[172:173], v[152:153], v[180:181]
	v_pk_mul_f32 v[110:111], v[110:111], v[162:163]
	s_waitcnt vmcnt(15)
	v_mov_b32_e32 v156, v214
	v_mov_b32_e32 v157, v215
	v_mov_b32_e32 v158, v216
	v_mov_b32_e32 v159, v217
	s_mul_i32 s98, s73, 0xa0
	v_add_u32_e32 v251, s98, v250
	global_load_dwordx4 v[214:217], v251, s[6:7]
	v_lshlrev_b32_e32 v9, 16, v156
	v_and_b32_e32 v11, 0xffff0000, v156
	v_lshlrev_b32_e32 v151, 16, v157
	v_and_b32_e32 v165, 0xffff0000, v157
	v_lshlrev_b32_e32 v13, 16, v158
	v_and_b32_e32 v163, 0xffff0000, v158
	v_lshlrev_b32_e32 v167, 16, v159
	v_and_b32_e32 v175, 0xffff0000, v159
	v_mul_f32_e32 v9, 0xbfb8aa3b, v9
	v_exp_f32_e32 v9, v9
	v_mul_f32_e32 v13, 0xbfb8aa3b, v13
	v_exp_f32_e32 v13, v13
	v_mul_f32_e32 v11, 0xbfb8aa3b, v11
	s_waitcnt vmcnt(15)
	v_mov_b32_e32 v168, v218
	v_mov_b32_e32 v169, v219
	v_mov_b32_e32 v170, v220
	v_mov_b32_e32 v171, v221
	s_mul_i32 s98, s73, 0xa0
	v_add_u32_e32 v251, s98, v250
	global_load_dwordx4 v[218:221], v251, s[8:9]
	v_lshlrev_b32_e32 v162, 16, v170
	v_add_f32_e32 v9, 1.0, v9
	v_exp_f32_e32 v11, v11
	v_rcp_f32_e32 v160, v9
	v_mul_f32_e32 v9, 0xbfb8aa3b, v162
	v_and_b32_e32 v161, 0xffff0000, v168
	v_exp_f32_e32 v162, v9
	v_add_f32_e32 v9, 1.0, v13
	v_lshlrev_b32_e32 v12, 16, v168
	v_rcp_f32_e32 v168, v9
	v_mul_f32_e32 v9, 0xbfb8aa3b, v161
	v_exp_f32_e32 v13, v9
	v_add_f32_e32 v9, 1.0, v11
	v_mul_f32_e32 v11, 0xbfb8aa3b, v163
	v_exp_f32_e32 v11, v11
	v_pk_mul_f32 v[112:113], v[112:113], v[172:173]
	v_lshlrev_b32_e32 v172, 16, v169
	v_and_b32_e32 v173, 0xffff0000, v169
	v_and_b32_e32 v169, 0xffff0000, v170
	v_rcp_f32_e32 v161, v9
	v_mul_f32_e32 v9, 0xbfb8aa3b, v169
	v_exp_f32_e32 v163, v9
	v_add_f32_e32 v9, 1.0, v11
	v_mul_f32_e32 v11, 0xbfb8aa3b, v151
	v_exp_f32_e32 v11, v11
	v_rcp_f32_e32 v169, v9
	v_mul_f32_e32 v9, 0xbfb8aa3b, v172
	v_exp_f32_e32 v170, v9
	v_add_f32_e32 v9, 1.0, v11
	v_mul_f32_e32 v11, 0xbfb8aa3b, v167
	v_exp_f32_e32 v11, v11
	v_lshlrev_b32_e32 v174, 16, v171
	v_rcp_f32_e32 v172, v9
	v_mul_f32_e32 v9, 0xbfb8aa3b, v174
	v_exp_f32_e32 v174, v9
	v_add_f32_e32 v9, 1.0, v11
	v_mul_f32_e32 v11, 0xbfb8aa3b, v165
	v_exp_f32_e32 v11, v11
	v_rcp_f32_e32 v176, v9
	v_mul_f32_e32 v151, 0xbfb8aa3b, v173
	v_mul_f32_e32 v12, 0xbfb8aa3b, v12
	v_add_f32_e32 v9, 1.0, v11
	v_rcp_f32_e32 v173, v9
	v_mul_f32_e32 v9, 0xbfb8aa3b, v175
	v_exp_f32_e32 v9, v9
	v_and_b32_e32 v177, 0xffff0000, v171
	v_exp_f32_e32 v12, v12
	v_mul_f32_e32 v11, 0xbfb8aa3b, v177
	v_exp_f32_e32 v171, v151
	v_exp_f32_e32 v175, v11
	v_add_f32_e32 v9, 1.0, v9
	v_rcp_f32_e32 v177, v9
	v_pk_add_f32 v[12:13], v[12:13], 1.0 op_sel_hi:[1,0]
	v_pk_add_f32 v[170:171], v[170:171], 1.0 op_sel_hi:[1,0]
	v_pk_mul_f32 v[12:13], v[12:13], v[160:161]
	v_pk_mul_f32 v[160:161], v[170:171], v[172:173]
	v_pk_mul_f32 v[106:107], v[106:107], v[12:13]
	v_pk_add_f32 v[12:13], v[174:175], 1.0 op_sel_hi:[1,0]
	v_add_u32_e32 v151, 48, v8
	v_pk_mul_f32 v[12:13], v[12:13], v[176:177]
	v_pk_mul_f32 v[108:109], v[108:109], v[160:161]
	v_pk_add_f32 v[160:161], v[162:163], 1.0 op_sel_hi:[1,0]
	v_pk_mul_f32 v[104:105], v[104:105], v[12:13]
	v_mad_i64_i32 v[12:13], s[26:27], v151, s73, v[4:5]
	v_pk_mul_f32 v[160:161], v[160:161], v[168:169]
	v_lshl_add_u64 v[12:13], v[12:13], 0, v[2:3]
	v_pk_mul_f32 v[102:103], v[102:103], v[160:161]
	s_waitcnt vmcnt(15)
; __device__ __forceinline__ void unpack8(u32x4 w, f32x4& a, f32x4& b) { a = (f32x4){bflo(w.x), bfhi(w.x), bflo(w.y), bfhi(w.y)}; b = (f32x4){bflo(w.z), bfhi(w.z), bflo(w.w), bfhi(w.w)}; }
;     __device__ __forceinline__ void mid(Acc& acc, const Unit& u, int wr, int wc, int fr, int fq) const {
;         const int row0 = u.row0 + wr * 64 + fr, col0 = u.col0 + wc * 32 + 8 * fq;
; #pragma unroll
;         for (int ai = 0; ai < 2; ++ai)
; #pragma unroll
;             for (int m = 0; m < 4; ++m) { const size_t ro = (size_t)(row0 + ai * HALF + m * 16) * ldg;
; #pragma unroll
;                 for (int bj = 0; bj < 2; ++bj) { const int col = col0 + bj * HALF;
;                     f32x4 a0, a1, b0, b1; unpack8(*(const u32x4*)(GA + ro + col), a0, a1); unpack8(*(const u32x4*)(GB + ro + col), b0, b1);
; #pragma unroll
;                     for (int j = 0; j < 4; ++j) { acc[ai][bj][m][0][j] *= (1.0f + __expf(-b0[j])) * __builtin_amdgcn_rcpf(1.0f + __expf(-a0[j])); acc[ai][bj][m][1][j] *= (1.0f + __expf(-b1[j])) * __builtin_amdgcn_rcpf(1.0f + __expf(-a1[j])); } } }
; template <class Epi, class Sched, bool F8 = false, bool MID = false, bool GATHER = false>
; __device__ __forceinline__ void gemm_phase(LAS unsigned char* lds, const Gemm g, const Sched& S, const Epi& E) {
;     ...
;             if constexpr (MID) { if (t == (nt >> 1)) { if constexpr (F8) asm volatile("s_nop 15\n\ts_nop 15" ::: "memory"); int l_; asm volatile("v_mbcnt_lo_u32_b32 %0, -1, 0\n\tv_mbcnt_hi_u32_b32 %0, -1, %0" : "=v"(l_)); E.mid(acc, cur, wr, wc, l_ & 15, l_ >> 4); if constexpr (F8) asm volatile("s_nop 7" ::: "memory"); } }
	v_mov_b32_e32 v152, v222
	v_mov_b32_e32 v153, v223
	v_mov_b32_e32 v154, v224
	v_mov_b32_e32 v155, v225
	s_mul_i32 s98, s73, 0xa0
	v_add_u32_e32 v251, s98, v250
	global_load_dwordx4 v[222:225], v251, s[6:7] offset:256
	v_lshlrev_b32_e32 v9, 16, v152
	v_and_b32_e32 v11, 0xffff0000, v152
	v_lshlrev_b32_e32 v165, 16, v153
	v_and_b32_e32 v167, 0xffff0000, v153
	v_mad_i64_i32 v[152:153], s[26:27], v151, s73, v[6:7]
	v_lshl_add_u64 v[172:173], v[152:153], 0, v[2:3]
	v_mul_f32_e32 v9, 0xbfb8aa3b, v9
	v_lshlrev_b32_e32 v174, 16, v154
	v_exp_f32_e32 v9, v9
	v_and_b32_e32 v175, 0xffff0000, v154
	v_mul_f32_e32 v154, 0xbfb8aa3b, v174
	v_lshlrev_b32_e32 v176, 16, v155
	v_and_b32_e32 v151, 0xffff0000, v155
	s_waitcnt vmcnt(15)
	v_mov_b32_e32 v156, v226
	v_mov_b32_e32 v157, v227
	v_mov_b32_e32 v158, v228
	v_mov_b32_e32 v159, v229
	s_mul_i32 s98, s73, 0xa0
	v_add_u32_e32 v251, s98, v250
	global_load_dwordx4 v[226:229], v251, s[8:9] offset:256
	v_lshlrev_b32_e32 v177, 16, v157
	v_and_b32_e32 v179, 0xffff0000, v157
	v_lshlrev_b32_e32 v155, 16, v158
	v_and_b32_e32 v157, 0xffff0000, v158
	v_exp_f32_e32 v158, v154
	v_mul_f32_e32 v11, 0xbfb8aa3b, v11
	v_add_f32_e32 v9, 1.0, v9
	v_exp_f32_e32 v11, v11
	v_rcp_f32_e32 v154, v9
	v_mul_f32_e32 v9, 0xbfb8aa3b, v155
	v_lshlrev_b32_e32 v152, 16, v156
	v_and_b32_e32 v153, 0xffff0000, v156
	v_exp_f32_e32 v156, v9
	v_add_f32_e32 v9, 1.0, v158
	v_rcp_f32_e32 v158, v9
	v_mul_f32_e32 v9, 0xbfb8aa3b, v153
	v_exp_f32_e32 v153, v9
	v_add_f32_e32 v9, 1.0, v11
	v_mul_f32_e32 v11, 0xbfb8aa3b, v175
	v_exp_f32_e32 v11, v11
	v_rcp_f32_e32 v155, v9
	v_mul_f32_e32 v9, 0xbfb8aa3b, v157
	v_exp_f32_e32 v157, v9
	v_add_f32_e32 v9, 1.0, v11
	v_mul_f32_e32 v11, 0xbfb8aa3b, v165
	v_exp_f32_e32 v11, v11
	v_lshlrev_b32_e32 v178, 16, v159
	v_and_b32_e32 v181, 0xffff0000, v159
	v_rcp_f32_e32 v159, v9
	v_mul_f32_e32 v9, 0xbfb8aa3b, v177
	v_exp_f32_e32 v174, v9
	v_add_f32_e32 v9, 1.0, v11
	v_mul_f32_e32 v11, 0xbfb8aa3b, v176
	v_exp_f32_e32 v11, v11
	v_rcp_f32_e32 v176, v9
	v_mul_f32_e32 v9, 0xbfb8aa3b, v178
	v_exp_f32_e32 v178, v9
	v_add_f32_e32 v9, 1.0, v11
	v_mul_f32_e32 v11, 0xbfb8aa3b, v167
	v_exp_f32_e32 v11, v11
	v_rcp_f32_e32 v180, v9
	v_mul_f32_e32 v152, 0xbfb8aa3b, v152
	v_mul_f32_e32 v165, 0xbfb8aa3b, v179
	v_add_f32_e32 v9, 1.0, v11
	v_rcp_f32_e32 v177, v9
	v_mul_f32_e32 v9, 0xbfb8aa3b, v151
	v_exp_f32_e32 v9, v9
	v_exp_f32_e32 v152, v152
	v_exp_f32_e32 v175, v165
	v_mul_f32_e32 v11, 0xbfb8aa3b, v181
	v_exp_f32_e32 v179, v11
	v_add_f32_e32 v9, 1.0, v9
	v_rcp_f32_e32 v181, v9
	v_pk_add_f32 v[174:175], v[174:175], 1.0 op_sel_hi:[1,0]
	v_pk_add_f32 v[152:153], v[152:153], 1.0 op_sel_hi:[1,0]
	s_nop 0
	v_pk_mul_f32 v[152:153], v[152:153], v[154:155]
	v_pk_mul_f32 v[154:155], v[174:175], v[176:177]
	v_pk_mul_f32 v[98:99], v[98:99], v[152:153]
	v_pk_mul_f32 v[100:101], v[100:101], v[154:155]
	v_pk_add_f32 v[152:153], v[178:179], 1.0 op_sel_hi:[1,0]
	v_pk_add_f32 v[154:155], v[156:157], 1.0 op_sel_hi:[1,0]
	s_nop 0
	v_pk_mul_f32 v[156:157], v[154:155], v[158:159]
	v_pk_mul_f32 v[158:159], v[152:153], v[180:181]
	v_pk_mul_f32 v[96:97], v[96:97], v[158:159]
	v_pk_mul_f32 v[94:95], v[94:95], v[156:157]
	s_waitcnt vmcnt(15)
	v_mov_b32_e32 v160, v230
	v_mov_b32_e32 v161, v231
	v_mov_b32_e32 v162, v232
	v_mov_b32_e32 v163, v233
	s_mul_i32 s98, s73, 0xb0
	v_add_u32_e32 v251, s98, v250
	global_load_dwordx4 v[230:233], v251, s[6:7]
	v_lshlrev_b32_e32 v9, 16, v160
	v_mul_f32_e32 v9, 0xbfb8aa3b, v9
	v_lshlrev_b32_e32 v13, 16, v162
	v_exp_f32_e32 v9, v9
	v_mul_f32_e32 v13, 0xbfb8aa3b, v13
	v_and_b32_e32 v11, 0xffff0000, v160
	v_exp_f32_e32 v13, v13
	v_mul_f32_e32 v11, 0xbfb8aa3b, v11
	v_lshlrev_b32_e32 v151, 16, v161
	v_and_b32_e32 v165, 0xffff0000, v161
	v_and_b32_e32 v161, 0xffff0000, v162
	s_waitcnt vmcnt(15)
	v_mov_b32_e32 v168, v234
	v_mov_b32_e32 v169, v235
	v_mov_b32_e32 v170, v236
	v_mov_b32_e32 v171, v237
	s_mul_i32 s98, s73, 0xb0
	v_add_u32_e32 v251, s98, v250
	global_load_dwordx4 v[234:237], v251, s[8:9]
	v_lshlrev_b32_e32 v162, 16, v170
	v_add_f32_e32 v9, 1.0, v9
	v_exp_f32_e32 v11, v11
	v_rcp_f32_e32 v160, v9
	v_mul_f32_e32 v9, 0xbfb8aa3b, v162
	v_lshlrev_b32_e32 v167, 16, v163
	v_and_b32_e32 v175, 0xffff0000, v163
	v_and_b32_e32 v163, 0xffff0000, v168
	v_exp_f32_e32 v162, v9
	v_add_f32_e32 v9, 1.0, v13
	v_lshlrev_b32_e32 v12, 16, v168
	v_rcp_f32_e32 v168, v9
	v_mul_f32_e32 v9, 0xbfb8aa3b, v163
	v_exp_f32_e32 v13, v9
	v_add_f32_e32 v9, 1.0, v11
	v_mul_f32_e32 v11, 0xbfb8aa3b, v161
	v_exp_f32_e32 v11, v11
	v_lshlrev_b32_e32 v172, 16, v169
	v_and_b32_e32 v173, 0xffff0000, v169
	v_and_b32_e32 v169, 0xffff0000, v170
	v_rcp_f32_e32 v161, v9
	v_mul_f32_e32 v9, 0xbfb8aa3b, v169
	v_exp_f32_e32 v163, v9
	v_add_f32_e32 v9, 1.0, v11
	v_mul_f32_e32 v11, 0xbfb8aa3b, v151
	v_exp_f32_e32 v11, v11
	v_rcp_f32_e32 v169, v9
	v_mul_f32_e32 v9, 0xbfb8aa3b, v172
	v_exp_f32_e32 v170, v9
	v_add_f32_e32 v9, 1.0, v11
	v_mul_f32_e32 v11, 0xbfb8aa3b, v167
	v_exp_f32_e32 v11, v11
	v_lshlrev_b32_e32 v174, 16, v171
	v_rcp_f32_e32 v172, v9
	v_mul_f32_e32 v9, 0xbfb8aa3b, v174
	v_exp_f32_e32 v174, v9
	v_add_f32_e32 v9, 1.0, v11
	v_mul_f32_e32 v11, 0xbfb8aa3b, v165
	v_exp_f32_e32 v11, v11
	v_rcp_f32_e32 v176, v9
	v_mul_f32_e32 v151, 0xbfb8aa3b, v173
	v_mul_f32_e32 v12, 0xbfb8aa3b, v12
	v_add_f32_e32 v9, 1.0, v11
	v_rcp_f32_e32 v173, v9
	v_mul_f32_e32 v9, 0xbfb8aa3b, v175
	v_exp_f32_e32 v9, v9
	v_and_b32_e32 v177, 0xffff0000, v171
	v_exp_f32_e32 v12, v12
	v_mul_f32_e32 v11, 0xbfb8aa3b, v177
	v_exp_f32_e32 v171, v151
	v_exp_f32_e32 v175, v11
	v_add_f32_e32 v9, 1.0, v9
	v_rcp_f32_e32 v177, v9
	v_pk_add_f32 v[12:13], v[12:13], 1.0 op_sel_hi:[1,0]
	v_pk_add_f32 v[170:171], v[170:171], 1.0 op_sel_hi:[1,0]
	v_pk_mul_f32 v[12:13], v[12:13], v[160:161]
	v_pk_mul_f32 v[160:161], v[170:171], v[172:173]
	v_pk_mul_f32 v[90:91], v[90:91], v[12:13]
	v_pk_add_f32 v[12:13], v[174:175], 1.0 op_sel_hi:[1,0]
	v_add_u32_e32 v151, 0x80, v8
	v_pk_mul_f32 v[12:13], v[12:13], v[176:177]
	v_pk_mul_f32 v[92:93], v[92:93], v[160:161]
	v_pk_add_f32 v[160:161], v[162:163], 1.0 op_sel_hi:[1,0]
	v_pk_mul_f32 v[88:89], v[88:89], v[12:13]
	v_mad_i64_i32 v[12:13], s[26:27], v151, s73, v[4:5]
	v_pk_mul_f32 v[160:161], v[160:161], v[168:169]
	v_lshl_add_u64 v[12:13], v[12:13], 0, v[2:3]
	v_pk_mul_f32 v[86:87], v[86:87], v[160:161]
	s_waitcnt vmcnt(15)
; __device__ __forceinline__ void unpack8(u32x4 w, f32x4& a, f32x4& b) { a = (f32x4){bflo(w.x), bfhi(w.x), bflo(w.y), bfhi(w.y)}; b = (f32x4){bflo(w.z), bfhi(w.z), bflo(w.w), bfhi(w.w)}; }
;     __device__ __forceinline__ void mid(Acc& acc, const Unit& u, int wr, int wc, int fr, int fq) const {
;         const int row0 = u.row0 + wr * 64 + fr, col0 = u.col0 + wc * 32 + 8 * fq;
; #pragma unroll
;         for (int ai = 0; ai < 2; ++ai)
; #pragma unroll
;             for (int m = 0; m < 4; ++m) { const size_t ro = (size_t)(row0 + ai * HALF + m * 16) * ldg;
; #pragma unroll
;                 for (int bj = 0; bj < 2; ++bj) { const int col = col0 + bj * HALF;
;                     f32x4 a0, a1, b0, b1; unpack8(*(const u32x4*)(GA + ro + col), a0, a1); unpack8(*(const u32x4*)(GB + ro + col), b0, b1);
; #pragma unroll
;                     for (int j = 0; j < 4; ++j) { acc[ai][bj][m][0][j] *= (1.0f + __expf(-b0[j])) * __builtin_amdgcn_rcpf(1.0f + __expf(-a0[j])); acc[ai][bj][m][1][j] *= (1.0f + __expf(-b1[j])) * __builtin_amdgcn_rcpf(1.0f + __expf(-a1[j])); } } }
; template <class Epi, class Sched, bool F8 = false, bool MID = false, bool GATHER = false>
; __device__ __forceinline__ void gemm_phase(LAS unsigned char* lds, const Gemm g, const Sched& S, const Epi& E) {
;     ...
;             if constexpr (MID) { if (t == (nt >> 1)) { if constexpr (F8) asm volatile("s_nop 15\n\ts_nop 15" ::: "memory"); int l_; asm volatile("v_mbcnt_lo_u32_b32 %0, -1, 0\n\tv_mbcnt_hi_u32_b32 %0, -1, %0" : "=v"(l_)); E.mid(acc, cur, wr, wc, l_ & 15, l_ >> 4); if constexpr (F8) asm volatile("s_nop 7" ::: "memory"); } }
	v_mov_b32_e32 v152, v238
	v_mov_b32_e32 v153, v239
	v_mov_b32_e32 v154, v240
	v_mov_b32_e32 v155, v241
	s_mul_i32 s98, s73, 0xb0
	v_add_u32_e32 v251, s98, v250
	global_load_dwordx4 v[238:241], v251, s[6:7] offset:256
	v_lshlrev_b32_e32 v9, 16, v152
	v_and_b32_e32 v11, 0xffff0000, v152
	v_lshlrev_b32_e32 v165, 16, v153
	v_and_b32_e32 v167, 0xffff0000, v153
	v_mad_i64_i32 v[152:153], s[26:27], v151, s73, v[6:7]
	v_lshl_add_u64 v[172:173], v[152:153], 0, v[2:3]
	v_mul_f32_e32 v9, 0xbfb8aa3b, v9
	v_lshlrev_b32_e32 v174, 16, v154
	v_exp_f32_e32 v9, v9
	v_and_b32_e32 v175, 0xffff0000, v154
	v_mul_f32_e32 v154, 0xbfb8aa3b, v174
	v_lshlrev_b32_e32 v176, 16, v155
	v_and_b32_e32 v151, 0xffff0000, v155
	s_waitcnt vmcnt(15)
	v_mov_b32_e32 v156, v242
	v_mov_b32_e32 v157, v243
	v_mov_b32_e32 v158, v244
	v_mov_b32_e32 v159, v245
	s_mul_i32 s98, s73, 0xb0
	v_add_u32_e32 v251, s98, v250
	global_load_dwordx4 v[242:245], v251, s[8:9] offset:256
	v_lshlrev_b32_e32 v177, 16, v157
	v_and_b32_e32 v179, 0xffff0000, v157
	v_lshlrev_b32_e32 v155, 16, v158
	v_and_b32_e32 v157, 0xffff0000, v158
	v_exp_f32_e32 v158, v154
	v_mul_f32_e32 v11, 0xbfb8aa3b, v11
	v_add_f32_e32 v9, 1.0, v9
	v_exp_f32_e32 v11, v11
	v_rcp_f32_e32 v154, v9
	v_mul_f32_e32 v9, 0xbfb8aa3b, v155
	v_lshlrev_b32_e32 v152, 16, v156
	v_and_b32_e32 v153, 0xffff0000, v156
	v_exp_f32_e32 v156, v9
	v_add_f32_e32 v9, 1.0, v158
	v_rcp_f32_e32 v158, v9
	v_mul_f32_e32 v9, 0xbfb8aa3b, v153
	v_exp_f32_e32 v153, v9
	v_add_f32_e32 v9, 1.0, v11
	v_mul_f32_e32 v11, 0xbfb8aa3b, v175
	v_exp_f32_e32 v11, v11
	v_rcp_f32_e32 v155, v9
	v_mul_f32_e32 v9, 0xbfb8aa3b, v157
	v_exp_f32_e32 v157, v9
	v_add_f32_e32 v9, 1.0, v11
	v_mul_f32_e32 v11, 0xbfb8aa3b, v165
	v_exp_f32_e32 v11, v11
	v_lshlrev_b32_e32 v178, 16, v159
	v_and_b32_e32 v181, 0xffff0000, v159
	v_rcp_f32_e32 v159, v9
	v_mul_f32_e32 v9, 0xbfb8aa3b, v177
	v_exp_f32_e32 v174, v9
	v_add_f32_e32 v9, 1.0, v11
	v_mul_f32_e32 v11, 0xbfb8aa3b, v176
	v_exp_f32_e32 v11, v11
	v_rcp_f32_e32 v176, v9
	v_mul_f32_e32 v9, 0xbfb8aa3b, v178
	v_exp_f32_e32 v178, v9
	v_add_f32_e32 v9, 1.0, v11
	v_mul_f32_e32 v11, 0xbfb8aa3b, v167
	v_exp_f32_e32 v11, v11
	v_rcp_f32_e32 v180, v9
	v_mul_f32_e32 v152, 0xbfb8aa3b, v152
	v_mul_f32_e32 v165, 0xbfb8aa3b, v179
	v_add_f32_e32 v9, 1.0, v11
	v_rcp_f32_e32 v177, v9
	v_mul_f32_e32 v9, 0xbfb8aa3b, v151
	v_exp_f32_e32 v9, v9
	v_exp_f32_e32 v152, v152
	v_exp_f32_e32 v175, v165
	v_mul_f32_e32 v11, 0xbfb8aa3b, v181
	v_exp_f32_e32 v179, v11
	v_add_f32_e32 v9, 1.0, v9
	v_rcp_f32_e32 v181, v9
	v_pk_add_f32 v[174:175], v[174:175], 1.0 op_sel_hi:[1,0]
	v_pk_add_f32 v[152:153], v[152:153], 1.0 op_sel_hi:[1,0]
	s_nop 0
	v_pk_mul_f32 v[152:153], v[152:153], v[154:155]
	v_pk_mul_f32 v[154:155], v[174:175], v[176:177]
	v_pk_mul_f32 v[82:83], v[82:83], v[152:153]
	v_pk_mul_f32 v[84:85], v[84:85], v[154:155]
	v_pk_add_f32 v[152:153], v[178:179], 1.0 op_sel_hi:[1,0]
	v_pk_add_f32 v[154:155], v[156:157], 1.0 op_sel_hi:[1,0]
	s_nop 0
	v_pk_mul_f32 v[156:157], v[154:155], v[158:159]
	v_pk_mul_f32 v[158:159], v[152:153], v[180:181]
	v_pk_mul_f32 v[80:81], v[80:81], v[158:159]
	v_pk_mul_f32 v[78:79], v[78:79], v[156:157]
	s_waitcnt vmcnt(15)
	v_mov_b32_e32 v160, v182
	v_mov_b32_e32 v161, v183
	v_mov_b32_e32 v162, v184
	v_mov_b32_e32 v163, v185
	v_lshlrev_b32_e32 v9, 16, v160
	v_mul_f32_e32 v9, 0xbfb8aa3b, v9
	v_lshlrev_b32_e32 v13, 16, v162
	v_exp_f32_e32 v9, v9
	v_mul_f32_e32 v13, 0xbfb8aa3b, v13
	v_and_b32_e32 v11, 0xffff0000, v160
	v_exp_f32_e32 v13, v13
	v_mul_f32_e32 v11, 0xbfb8aa3b, v11
	v_lshlrev_b32_e32 v151, 16, v161
	v_and_b32_e32 v165, 0xffff0000, v161
	v_and_b32_e32 v161, 0xffff0000, v162
	s_waitcnt vmcnt(14)
	v_mov_b32_e32 v168, v186
	v_mov_b32_e32 v169, v187
	v_mov_b32_e32 v170, v188
	v_mov_b32_e32 v171, v189
	v_lshlrev_b32_e32 v162, 16, v170
	v_add_f32_e32 v9, 1.0, v9
	v_exp_f32_e32 v11, v11
	v_rcp_f32_e32 v160, v9
	v_mul_f32_e32 v9, 0xbfb8aa3b, v162
	v_lshlrev_b32_e32 v167, 16, v163
	v_and_b32_e32 v175, 0xffff0000, v163
	v_and_b32_e32 v163, 0xffff0000, v168
	v_exp_f32_e32 v162, v9
	v_add_f32_e32 v9, 1.0, v13
	v_lshlrev_b32_e32 v12, 16, v168
	v_rcp_f32_e32 v168, v9
	v_mul_f32_e32 v9, 0xbfb8aa3b, v163
	v_exp_f32_e32 v13, v9
	v_add_f32_e32 v9, 1.0, v11
	v_mul_f32_e32 v11, 0xbfb8aa3b, v161
	v_exp_f32_e32 v11, v11
	v_lshlrev_b32_e32 v172, 16, v169
	v_and_b32_e32 v173, 0xffff0000, v169
	v_and_b32_e32 v169, 0xffff0000, v170
	v_rcp_f32_e32 v161, v9
	v_mul_f32_e32 v9, 0xbfb8aa3b, v169
	v_exp_f32_e32 v163, v9
	v_add_f32_e32 v9, 1.0, v11
	v_mul_f32_e32 v11, 0xbfb8aa3b, v151
	v_exp_f32_e32 v11, v11
	v_rcp_f32_e32 v169, v9
	v_mul_f32_e32 v9, 0xbfb8aa3b, v172
	v_exp_f32_e32 v170, v9
	v_add_f32_e32 v9, 1.0, v11
	v_mul_f32_e32 v11, 0xbfb8aa3b, v167
	v_exp_f32_e32 v11, v11
	v_lshlrev_b32_e32 v174, 16, v171
	v_rcp_f32_e32 v172, v9
	v_mul_f32_e32 v9, 0xbfb8aa3b, v174
	v_exp_f32_e32 v174, v9
	v_add_f32_e32 v9, 1.0, v11
	v_mul_f32_e32 v11, 0xbfb8aa3b, v165
	v_exp_f32_e32 v11, v11
	v_rcp_f32_e32 v176, v9
	v_mul_f32_e32 v151, 0xbfb8aa3b, v173
	v_mul_f32_e32 v12, 0xbfb8aa3b, v12
	v_add_f32_e32 v9, 1.0, v11
	v_rcp_f32_e32 v173, v9
	v_mul_f32_e32 v9, 0xbfb8aa3b, v175
	v_exp_f32_e32 v9, v9
	v_and_b32_e32 v177, 0xffff0000, v171
	v_exp_f32_e32 v12, v12
	v_mul_f32_e32 v11, 0xbfb8aa3b, v177
	v_exp_f32_e32 v171, v151
	v_exp_f32_e32 v175, v11
	v_add_f32_e32 v9, 1.0, v9
	v_rcp_f32_e32 v177, v9
	v_pk_add_f32 v[12:13], v[12:13], 1.0 op_sel_hi:[1,0]
	v_pk_add_f32 v[170:171], v[170:171], 1.0 op_sel_hi:[1,0]
	v_pk_mul_f32 v[12:13], v[12:13], v[160:161]
	v_pk_mul_f32 v[160:161], v[170:171], v[172:173]
	v_pk_mul_f32 v[74:75], v[74:75], v[12:13]
	v_pk_add_f32 v[12:13], v[174:175], 1.0 op_sel_hi:[1,0]
	v_add_u32_e32 v151, 0x90, v8
	v_pk_mul_f32 v[12:13], v[12:13], v[176:177]
	v_pk_mul_f32 v[76:77], v[76:77], v[160:161]
	v_pk_add_f32 v[160:161], v[162:163], 1.0 op_sel_hi:[1,0]
	v_pk_mul_f32 v[72:73], v[72:73], v[12:13]
	v_mad_i64_i32 v[12:13], s[26:27], v151, s73, v[4:5]
	v_pk_mul_f32 v[160:161], v[160:161], v[168:169]
	v_lshl_add_u64 v[12:13], v[12:13], 0, v[2:3]
	v_pk_mul_f32 v[70:71], v[70:71], v[160:161]
	s_waitcnt vmcnt(13)
; __device__ __forceinline__ void unpack8(u32x4 w, f32x4& a, f32x4& b) { a = (f32x4){bflo(w.x), bfhi(w.x), bflo(w.y), bfhi(w.y)}; b = (f32x4){bflo(w.z), bfhi(w.z), bflo(w.w), bfhi(w.w)}; }
;     __device__ __forceinline__ void mid(Acc& acc, const Unit& u, int wr, int wc, int fr, int fq) const {
;         const int row0 = u.row0 + wr * 64 + fr, col0 = u.col0 + wc * 32 + 8 * fq;
; #pragma unroll
;         for (int ai = 0; ai < 2; ++ai)
; #pragma unroll
;             for (int m = 0; m < 4; ++m) { const size_t ro = (size_t)(row0 + ai * HALF + m * 16) * ldg;
; #pragma unroll
;                 for (int bj = 0; bj < 2; ++bj) { const int col = col0 + bj * HALF;
;                     f32x4 a0, a1, b0, b1; unpack8(*(const u32x4*)(GA + ro + col), a0, a1); unpack8(*(const u32x4*)(GB + ro + col), b0, b1);
; #pragma unroll
;                     for (int j = 0; j < 4; ++j) { acc[ai][bj][m][0][j] *= (1.0f + __expf(-b0[j])) * __builtin_amdgcn_rcpf(1.0f + __expf(-a0[j])); acc[ai][bj][m][1][j] *= (1.0f + __expf(-b1[j])) * __builtin_amdgcn_rcpf(1.0f + __expf(-a1[j])); } } }
; template <class Epi, class Sched, bool F8 = false, bool MID = false, bool GATHER = false>
; __device__ __forceinline__ void gemm_phase(LAS unsigned char* lds, const Gemm g, const Sched& S, const Epi& E) {
;     ...
;             if constexpr (MID) { if (t == (nt >> 1)) { if constexpr (F8) asm volatile("s_nop 15\n\ts_nop 15" ::: "memory"); int l_; asm volatile("v_mbcnt_lo_u32_b32 %0, -1, 0\n\tv_mbcnt_hi_u32_b32 %0, -1, %0" : "=v"(l_)); E.mid(acc, cur, wr, wc, l_ & 15, l_ >> 4); if constexpr (F8) asm volatile("s_nop 7" ::: "memory"); } }
	v_mov_b32_e32 v152, v190
	v_mov_b32_e32 v153, v191
	v_mov_b32_e32 v154, v192
	v_mov_b32_e32 v155, v193
	v_lshlrev_b32_e32 v9, 16, v152
	v_and_b32_e32 v11, 0xffff0000, v152
	v_lshlrev_b32_e32 v165, 16, v153
	v_and_b32_e32 v167, 0xffff0000, v153
	v_mad_i64_i32 v[152:153], s[26:27], v151, s73, v[6:7]
	v_mul_f32_e32 v9, 0xbfb8aa3b, v9
	v_lshlrev_b32_e32 v174, 16, v154
	v_lshl_add_u64 v[172:173], v[152:153], 0, v[2:3]
	v_exp_f32_e32 v9, v9
	v_and_b32_e32 v175, 0xffff0000, v154
	v_mul_f32_e32 v154, 0xbfb8aa3b, v174
	v_lshlrev_b32_e32 v176, 16, v155
	v_and_b32_e32 v151, 0xffff0000, v155
	s_waitcnt vmcnt(12)
	v_mov_b32_e32 v156, v194
	v_mov_b32_e32 v157, v195
	v_mov_b32_e32 v158, v196
	v_mov_b32_e32 v159, v197
	v_lshlrev_b32_e32 v177, 16, v157
	v_and_b32_e32 v179, 0xffff0000, v157
	v_lshlrev_b32_e32 v155, 16, v158
	v_and_b32_e32 v157, 0xffff0000, v158
	v_exp_f32_e32 v158, v154
	v_mul_f32_e32 v11, 0xbfb8aa3b, v11
	v_add_f32_e32 v9, 1.0, v9
	v_exp_f32_e32 v11, v11
	v_rcp_f32_e32 v154, v9
	v_mul_f32_e32 v9, 0xbfb8aa3b, v155
	v_lshlrev_b32_e32 v152, 16, v156
	v_and_b32_e32 v153, 0xffff0000, v156
	v_exp_f32_e32 v156, v9
	v_add_f32_e32 v9, 1.0, v158
	v_rcp_f32_e32 v158, v9
	v_mul_f32_e32 v9, 0xbfb8aa3b, v153
	v_exp_f32_e32 v153, v9
	v_add_f32_e32 v9, 1.0, v11
	v_mul_f32_e32 v11, 0xbfb8aa3b, v175
	v_exp_f32_e32 v11, v11
	v_rcp_f32_e32 v155, v9
	v_mul_f32_e32 v9, 0xbfb8aa3b, v157
	v_exp_f32_e32 v157, v9
	v_add_f32_e32 v9, 1.0, v11
	v_mul_f32_e32 v11, 0xbfb8aa3b, v165
	v_exp_f32_e32 v11, v11
	v_lshlrev_b32_e32 v178, 16, v159
	v_and_b32_e32 v181, 0xffff0000, v159
	v_rcp_f32_e32 v159, v9
	v_mul_f32_e32 v9, 0xbfb8aa3b, v177
	v_exp_f32_e32 v174, v9
	v_add_f32_e32 v9, 1.0, v11
	v_mul_f32_e32 v11, 0xbfb8aa3b, v176
	v_exp_f32_e32 v11, v11
	v_rcp_f32_e32 v176, v9
	v_mul_f32_e32 v9, 0xbfb8aa3b, v178
	v_exp_f32_e32 v178, v9
	v_add_f32_e32 v9, 1.0, v11
	v_mul_f32_e32 v11, 0xbfb8aa3b, v167
	v_exp_f32_e32 v11, v11
	v_rcp_f32_e32 v180, v9
	v_mul_f32_e32 v152, 0xbfb8aa3b, v152
	v_mul_f32_e32 v165, 0xbfb8aa3b, v179
	v_add_f32_e32 v9, 1.0, v11
	v_rcp_f32_e32 v177, v9
	v_mul_f32_e32 v9, 0xbfb8aa3b, v151
	v_exp_f32_e32 v9, v9
	v_exp_f32_e32 v152, v152
	v_exp_f32_e32 v175, v165
	v_mul_f32_e32 v11, 0xbfb8aa3b, v181
	v_exp_f32_e32 v179, v11
	v_add_f32_e32 v9, 1.0, v9
	v_rcp_f32_e32 v181, v9
	v_pk_add_f32 v[174:175], v[174:175], 1.0 op_sel_hi:[1,0]
	v_pk_add_f32 v[152:153], v[152:153], 1.0 op_sel_hi:[1,0]
	s_nop 0
	v_pk_mul_f32 v[152:153], v[152:153], v[154:155]
	v_pk_mul_f32 v[154:155], v[174:175], v[176:177]
	v_pk_mul_f32 v[66:67], v[66:67], v[152:153]
	v_pk_mul_f32 v[68:69], v[68:69], v[154:155]
	v_pk_add_f32 v[152:153], v[178:179], 1.0 op_sel_hi:[1,0]
	v_pk_add_f32 v[154:155], v[156:157], 1.0 op_sel_hi:[1,0]
	s_nop 0
	v_pk_mul_f32 v[156:157], v[154:155], v[158:159]
	v_pk_mul_f32 v[158:159], v[152:153], v[180:181]
	v_pk_mul_f32 v[64:65], v[64:65], v[158:159]
	v_pk_mul_f32 v[62:63], v[62:63], v[156:157]
	s_waitcnt vmcnt(11)
	v_mov_b32_e32 v160, v198
	v_mov_b32_e32 v161, v199
	v_mov_b32_e32 v162, v200
	v_mov_b32_e32 v163, v201
	v_lshlrev_b32_e32 v9, 16, v160
	v_mul_f32_e32 v9, 0xbfb8aa3b, v9
	v_lshlrev_b32_e32 v13, 16, v162
	v_exp_f32_e32 v9, v9
	v_mul_f32_e32 v13, 0xbfb8aa3b, v13
	v_and_b32_e32 v11, 0xffff0000, v160
	v_exp_f32_e32 v13, v13
	v_mul_f32_e32 v11, 0xbfb8aa3b, v11
	v_lshlrev_b32_e32 v151, 16, v161
	v_and_b32_e32 v165, 0xffff0000, v161
	v_and_b32_e32 v161, 0xffff0000, v162
	s_waitcnt vmcnt(10)
	v_mov_b32_e32 v168, v202
	v_mov_b32_e32 v169, v203
	v_mov_b32_e32 v170, v204
	v_mov_b32_e32 v171, v205
	v_lshlrev_b32_e32 v162, 16, v170
	v_add_f32_e32 v9, 1.0, v9
	v_exp_f32_e32 v11, v11
	v_rcp_f32_e32 v160, v9
	v_mul_f32_e32 v9, 0xbfb8aa3b, v162
	v_lshlrev_b32_e32 v167, 16, v163
	v_and_b32_e32 v175, 0xffff0000, v163
	v_and_b32_e32 v163, 0xffff0000, v168
	v_exp_f32_e32 v162, v9
	v_add_f32_e32 v9, 1.0, v13
	v_lshlrev_b32_e32 v12, 16, v168
	v_rcp_f32_e32 v168, v9
	v_mul_f32_e32 v9, 0xbfb8aa3b, v163
	v_exp_f32_e32 v13, v9
	v_add_f32_e32 v9, 1.0, v11
	v_mul_f32_e32 v11, 0xbfb8aa3b, v161
	v_exp_f32_e32 v11, v11
	v_lshlrev_b32_e32 v172, 16, v169
	v_and_b32_e32 v173, 0xffff0000, v169
	v_and_b32_e32 v169, 0xffff0000, v170
	v_rcp_f32_e32 v161, v9
	v_mul_f32_e32 v9, 0xbfb8aa3b, v169
	v_exp_f32_e32 v163, v9
	v_add_f32_e32 v9, 1.0, v11
	v_mul_f32_e32 v11, 0xbfb8aa3b, v151
	v_exp_f32_e32 v11, v11
	v_rcp_f32_e32 v169, v9
	v_mul_f32_e32 v9, 0xbfb8aa3b, v172
	v_exp_f32_e32 v170, v9
	v_add_f32_e32 v9, 1.0, v11
	v_mul_f32_e32 v11, 0xbfb8aa3b, v167
	v_exp_f32_e32 v11, v11
	v_lshlrev_b32_e32 v174, 16, v171
	v_rcp_f32_e32 v172, v9
	v_mul_f32_e32 v9, 0xbfb8aa3b, v174
	v_exp_f32_e32 v174, v9
	v_add_f32_e32 v9, 1.0, v11
	v_mul_f32_e32 v11, 0xbfb8aa3b, v165
	v_exp_f32_e32 v11, v11
	v_rcp_f32_e32 v176, v9
	v_mul_f32_e32 v151, 0xbfb8aa3b, v173
	v_mul_f32_e32 v12, 0xbfb8aa3b, v12
	v_add_f32_e32 v9, 1.0, v11
	v_rcp_f32_e32 v173, v9
	v_mul_f32_e32 v9, 0xbfb8aa3b, v175
	v_exp_f32_e32 v9, v9
	v_and_b32_e32 v177, 0xffff0000, v171
	v_exp_f32_e32 v12, v12
	v_mul_f32_e32 v11, 0xbfb8aa3b, v177
	v_exp_f32_e32 v171, v151
	v_exp_f32_e32 v175, v11
	v_add_f32_e32 v9, 1.0, v9
	v_rcp_f32_e32 v177, v9
	v_pk_add_f32 v[12:13], v[12:13], 1.0 op_sel_hi:[1,0]
	v_pk_add_f32 v[170:171], v[170:171], 1.0 op_sel_hi:[1,0]
	v_pk_mul_f32 v[12:13], v[12:13], v[160:161]
	v_pk_mul_f32 v[160:161], v[170:171], v[172:173]
	v_pk_mul_f32 v[58:59], v[58:59], v[12:13]
	v_pk_add_f32 v[12:13], v[174:175], 1.0 op_sel_hi:[1,0]
	v_add_u32_e32 v151, 0xa0, v8
	v_pk_mul_f32 v[12:13], v[12:13], v[176:177]
	v_pk_mul_f32 v[60:61], v[60:61], v[160:161]
	v_pk_add_f32 v[160:161], v[162:163], 1.0 op_sel_hi:[1,0]
	v_pk_mul_f32 v[56:57], v[56:57], v[12:13]
	v_mad_i64_i32 v[12:13], s[26:27], v151, s73, v[4:5]
	v_pk_mul_f32 v[160:161], v[160:161], v[168:169]
	v_lshl_add_u64 v[12:13], v[12:13], 0, v[2:3]
	v_pk_mul_f32 v[54:55], v[54:55], v[160:161]
	s_waitcnt vmcnt(9)
; __device__ __forceinline__ void unpack8(u32x4 w, f32x4& a, f32x4& b) { a = (f32x4){bflo(w.x), bfhi(w.x), bflo(w.y), bfhi(w.y)}; b = (f32x4){bflo(w.z), bfhi(w.z), bflo(w.w), bfhi(w.w)}; }
;     __device__ __forceinline__ void mid(Acc& acc, const Unit& u, int wr, int wc, int fr, int fq) const {
;         const int row0 = u.row0 + wr * 64 + fr, col0 = u.col0 + wc * 32 + 8 * fq;
; #pragma unroll
;         for (int ai = 0; ai < 2; ++ai)
; #pragma unroll
;             for (int m = 0; m < 4; ++m) { const size_t ro = (size_t)(row0 + ai * HALF + m * 16) * ldg;
; #pragma unroll
;                 for (int bj = 0; bj < 2; ++bj) { const int col = col0 + bj * HALF;
;                     f32x4 a0, a1, b0, b1; unpack8(*(const u32x4*)(GA + ro + col), a0, a1); unpack8(*(const u32x4*)(GB + ro + col), b0, b1);
; #pragma unroll
;                     for (int j = 0; j < 4; ++j) { acc[ai][bj][m][0][j] *= (1.0f + __expf(-b0[j])) * __builtin_amdgcn_rcpf(1.0f + __expf(-a0[j])); acc[ai][bj][m][1][j] *= (1.0f + __expf(-b1[j])) * __builtin_amdgcn_rcpf(1.0f + __expf(-a1[j])); } } }
; template <class Epi, class Sched, bool F8 = false, bool MID = false, bool GATHER = false>
; __device__ __forceinline__ void gemm_phase(LAS unsigned char* lds, const Gemm g, const Sched& S, const Epi& E) {
;     ...
;             if constexpr (MID) { if (t == (nt >> 1)) { if constexpr (F8) asm volatile("s_nop 15\n\ts_nop 15" ::: "memory"); int l_; asm volatile("v_mbcnt_lo_u32_b32 %0, -1, 0\n\tv_mbcnt_hi_u32_b32 %0, -1, %0" : "=v"(l_)); E.mid(acc, cur, wr, wc, l_ & 15, l_ >> 4); if constexpr (F8) asm volatile("s_nop 7" ::: "memory"); } }
	v_mov_b32_e32 v152, v206
	v_mov_b32_e32 v153, v207
	v_mov_b32_e32 v154, v208
	v_mov_b32_e32 v155, v209
	v_lshlrev_b32_e32 v9, 16, v152
	v_mul_f32_e32 v9, 0xbfb8aa3b, v9
	v_lshlrev_b32_e32 v174, 16, v154
	v_exp_f32_e32 v9, v9
	v_and_b32_e32 v175, 0xffff0000, v154
	v_mul_f32_e32 v154, 0xbfb8aa3b, v174
	v_and_b32_e32 v11, 0xffff0000, v152
	v_lshlrev_b32_e32 v165, 16, v153
	v_and_b32_e32 v167, 0xffff0000, v153
	v_lshlrev_b32_e32 v176, 16, v155
	v_mad_i64_i32 v[152:153], s[26:27], v151, s73, v[6:7]
	v_and_b32_e32 v151, 0xffff0000, v155
	s_waitcnt vmcnt(8)
	v_mov_b32_e32 v156, v210
	v_mov_b32_e32 v157, v211
	v_mov_b32_e32 v158, v212
	v_mov_b32_e32 v159, v213
	v_lshlrev_b32_e32 v177, 16, v157
	v_and_b32_e32 v179, 0xffff0000, v157
	v_lshlrev_b32_e32 v155, 16, v158
	v_and_b32_e32 v157, 0xffff0000, v158
	v_exp_f32_e32 v158, v154
	v_lshl_add_u64 v[172:173], v[152:153], 0, v[2:3]
	v_mul_f32_e32 v11, 0xbfb8aa3b, v11
	v_add_f32_e32 v9, 1.0, v9
	v_exp_f32_e32 v11, v11
	v_rcp_f32_e32 v154, v9
	v_mul_f32_e32 v9, 0xbfb8aa3b, v155
	v_lshlrev_b32_e32 v152, 16, v156
	v_and_b32_e32 v153, 0xffff0000, v156
	v_exp_f32_e32 v156, v9
	v_add_f32_e32 v9, 1.0, v158
	v_rcp_f32_e32 v158, v9
	v_mul_f32_e32 v9, 0xbfb8aa3b, v153
	v_exp_f32_e32 v153, v9
	v_add_f32_e32 v9, 1.0, v11
	v_mul_f32_e32 v11, 0xbfb8aa3b, v175
	v_exp_f32_e32 v11, v11
	v_rcp_f32_e32 v155, v9
	v_mul_f32_e32 v9, 0xbfb8aa3b, v157
	v_exp_f32_e32 v157, v9
	v_add_f32_e32 v9, 1.0, v11
	v_mul_f32_e32 v11, 0xbfb8aa3b, v165
	v_exp_f32_e32 v11, v11
	v_lshlrev_b32_e32 v178, 16, v159
	v_and_b32_e32 v181, 0xffff0000, v159
	v_rcp_f32_e32 v159, v9
	v_mul_f32_e32 v9, 0xbfb8aa3b, v177
	v_exp_f32_e32 v174, v9
	v_add_f32_e32 v9, 1.0, v11
	v_mul_f32_e32 v11, 0xbfb8aa3b, v176
	v_exp_f32_e32 v11, v11
	v_rcp_f32_e32 v176, v9
	v_mul_f32_e32 v9, 0xbfb8aa3b, v178
	v_exp_f32_e32 v178, v9
	v_add_f32_e32 v9, 1.0, v11
	v_mul_f32_e32 v11, 0xbfb8aa3b, v167
	v_exp_f32_e32 v11, v11
	v_rcp_f32_e32 v180, v9
	v_mul_f32_e32 v152, 0xbfb8aa3b, v152
	v_mul_f32_e32 v165, 0xbfb8aa3b, v179
	v_add_f32_e32 v9, 1.0, v11
	v_rcp_f32_e32 v177, v9
	v_mul_f32_e32 v9, 0xbfb8aa3b, v151
	v_exp_f32_e32 v9, v9
	v_exp_f32_e32 v152, v152
	v_exp_f32_e32 v175, v165
	v_mul_f32_e32 v11, 0xbfb8aa3b, v181
	v_exp_f32_e32 v179, v11
	v_add_f32_e32 v9, 1.0, v9
	v_rcp_f32_e32 v181, v9
	v_pk_add_f32 v[174:175], v[174:175], 1.0 op_sel_hi:[1,0]
	v_pk_add_f32 v[152:153], v[152:153], 1.0 op_sel_hi:[1,0]
	s_nop 0
	v_pk_mul_f32 v[152:153], v[152:153], v[154:155]
	v_pk_mul_f32 v[154:155], v[174:175], v[176:177]
	v_pk_mul_f32 v[50:51], v[50:51], v[152:153]
	v_pk_mul_f32 v[52:53], v[52:53], v[154:155]
	v_pk_add_f32 v[152:153], v[178:179], 1.0 op_sel_hi:[1,0]
	v_pk_add_f32 v[154:155], v[156:157], 1.0 op_sel_hi:[1,0]
	s_nop 0
	v_pk_mul_f32 v[156:157], v[154:155], v[158:159]
	v_pk_mul_f32 v[158:159], v[152:153], v[180:181]
	v_pk_mul_f32 v[48:49], v[48:49], v[158:159]
	v_pk_mul_f32 v[46:47], v[46:47], v[156:157]
	s_waitcnt vmcnt(7)
	v_mov_b32_e32 v160, v214
	v_mov_b32_e32 v161, v215
	v_mov_b32_e32 v162, v216
	v_mov_b32_e32 v163, v217
	v_lshlrev_b32_e32 v9, 16, v160
	v_mul_f32_e32 v9, 0xbfb8aa3b, v9
	v_lshlrev_b32_e32 v13, 16, v162
	v_exp_f32_e32 v9, v9
	v_mul_f32_e32 v13, 0xbfb8aa3b, v13
	v_and_b32_e32 v11, 0xffff0000, v160
	v_exp_f32_e32 v13, v13
	v_mul_f32_e32 v11, 0xbfb8aa3b, v11
	v_lshlrev_b32_e32 v151, 16, v161
	v_and_b32_e32 v165, 0xffff0000, v161
	v_and_b32_e32 v161, 0xffff0000, v162
	v_add_f32_e32 v9, 1.0, v9
	v_exp_f32_e32 v11, v11
	v_rcp_f32_e32 v160, v9
	v_lshlrev_b32_e32 v167, 16, v163
	v_and_b32_e32 v175, 0xffff0000, v163
	s_waitcnt vmcnt(6)
	v_mov_b32_e32 v168, v218
	v_mov_b32_e32 v169, v219
	v_mov_b32_e32 v170, v220
	v_mov_b32_e32 v171, v221
	v_lshlrev_b32_e32 v162, 16, v170
	v_mul_f32_e32 v9, 0xbfb8aa3b, v162
	v_and_b32_e32 v163, 0xffff0000, v168
	v_exp_f32_e32 v162, v9
	v_add_f32_e32 v9, 1.0, v13
	v_lshlrev_b32_e32 v12, 16, v168
	v_rcp_f32_e32 v168, v9
	v_mul_f32_e32 v9, 0xbfb8aa3b, v163
	v_exp_f32_e32 v13, v9
	v_add_f32_e32 v9, 1.0, v11
	v_mul_f32_e32 v11, 0xbfb8aa3b, v161
	v_exp_f32_e32 v11, v11
	v_lshlrev_b32_e32 v172, 16, v169
	v_and_b32_e32 v173, 0xffff0000, v169
	v_and_b32_e32 v169, 0xffff0000, v170
	v_rcp_f32_e32 v161, v9
	v_mul_f32_e32 v9, 0xbfb8aa3b, v169
	v_exp_f32_e32 v163, v9
	v_add_f32_e32 v9, 1.0, v11
	v_mul_f32_e32 v11, 0xbfb8aa3b, v151
	v_exp_f32_e32 v11, v11
	v_rcp_f32_e32 v169, v9
	v_mul_f32_e32 v9, 0xbfb8aa3b, v172
	v_exp_f32_e32 v170, v9
	v_add_f32_e32 v9, 1.0, v11
	v_mul_f32_e32 v11, 0xbfb8aa3b, v167
	v_exp_f32_e32 v11, v11
	v_lshlrev_b32_e32 v174, 16, v171
	v_rcp_f32_e32 v172, v9
	v_mul_f32_e32 v9, 0xbfb8aa3b, v174
	v_exp_f32_e32 v174, v9
	v_add_f32_e32 v9, 1.0, v11
	v_mul_f32_e32 v11, 0xbfb8aa3b, v165
	v_exp_f32_e32 v11, v11
	v_rcp_f32_e32 v176, v9
	v_mul_f32_e32 v151, 0xbfb8aa3b, v173
	v_mul_f32_e32 v12, 0xbfb8aa3b, v12
	v_add_f32_e32 v9, 1.0, v11
	v_rcp_f32_e32 v173, v9
	v_mul_f32_e32 v9, 0xbfb8aa3b, v175
	v_exp_f32_e32 v9, v9
	v_and_b32_e32 v177, 0xffff0000, v171
	v_exp_f32_e32 v12, v12
	v_mul_f32_e32 v11, 0xbfb8aa3b, v177
	v_exp_f32_e32 v175, v11
	v_add_f32_e32 v9, 1.0, v9
	v_exp_f32_e32 v171, v151
	v_rcp_f32_e32 v177, v9
	v_pk_add_f32 v[12:13], v[12:13], 1.0 op_sel_hi:[1,0]
	v_pk_add_f32 v[170:171], v[170:171], 1.0 op_sel_hi:[1,0]
	v_pk_mul_f32 v[12:13], v[12:13], v[160:161]
	v_pk_mul_f32 v[160:161], v[170:171], v[172:173]
	v_pk_mul_f32 v[42:43], v[42:43], v[12:13]
	v_pk_add_f32 v[12:13], v[174:175], 1.0 op_sel_hi:[1,0]
	v_pk_mul_f32 v[44:45], v[44:45], v[160:161]
	v_pk_mul_f32 v[12:13], v[12:13], v[176:177]
	v_pk_add_f32 v[160:161], v[162:163], 1.0 op_sel_hi:[1,0]
	v_pk_mul_f32 v[40:41], v[40:41], v[12:13]
	v_add_u32_e32 v12, 0xb0, v8
	s_waitcnt vmcnt(5)
; __device__ __forceinline__ void unpack8(u32x4 w, f32x4& a, f32x4& b) { a = (f32x4){bflo(w.x), bfhi(w.x), bflo(w.y), bfhi(w.y)}; b = (f32x4){bflo(w.z), bfhi(w.z), bflo(w.w), bfhi(w.w)}; }
;     __device__ __forceinline__ void mid(Acc& acc, const Unit& u, int wr, int wc, int fr, int fq) const {
;         const int row0 = u.row0 + wr * 64 + fr, col0 = u.col0 + wc * 32 + 8 * fq;
; #pragma unroll
;         for (int ai = 0; ai < 2; ++ai)
; #pragma unroll
;             for (int m = 0; m < 4; ++m) { const size_t ro = (size_t)(row0 + ai * HALF + m * 16) * ldg;
; #pragma unroll
;                 for (int bj = 0; bj < 2; ++bj) { const int col = col0 + bj * HALF;
;                     f32x4 a0, a1, b0, b1; unpack8(*(const u32x4*)(GA + ro + col), a0, a1); unpack8(*(const u32x4*)(GB + ro + col), b0, b1);
; #pragma unroll
;                     for (int j = 0; j < 4; ++j) { acc[ai][bj][m][0][j] *= (1.0f + __expf(-b0[j])) * __builtin_amdgcn_rcpf(1.0f + __expf(-a0[j])); acc[ai][bj][m][1][j] *= (1.0f + __expf(-b1[j])) * __builtin_amdgcn_rcpf(1.0f + __expf(-a1[j])); } } }
; template <class Epi, class Sched, bool F8 = false, bool MID = false, bool GATHER = false>
; __device__ __forceinline__ void gemm_phase(LAS unsigned char* lds, const Gemm g, const Sched& S, const Epi& E) {
;     ...
;             if constexpr (MID) { if (t == (nt >> 1)) { if constexpr (F8) asm volatile("s_nop 15\n\ts_nop 15" ::: "memory"); int l_; asm volatile("v_mbcnt_lo_u32_b32 %0, -1, 0\n\tv_mbcnt_hi_u32_b32 %0, -1, %0" : "=v"(l_)); E.mid(acc, cur, wr, wc, l_ & 15, l_ >> 4); if constexpr (F8) asm volatile("s_nop 7" ::: "memory"); } }
	v_mov_b32_e32 v152, v222
	v_mov_b32_e32 v153, v223
	v_mov_b32_e32 v154, v224
	v_mov_b32_e32 v155, v225
	v_lshlrev_b32_e32 v11, 16, v152
	v_mul_f32_e32 v11, 0xbfb8aa3b, v11
	v_and_b32_e32 v151, 0xffff0000, v152
	v_mad_i64_i32 v[4:5], s[26:27], v12, s73, v[4:5]
	v_lshlrev_b32_e32 v152, 16, v154
	v_exp_f32_e32 v11, v11
	v_pk_mul_f32 v[160:161], v[160:161], v[168:169]
	v_lshl_add_u64 v[8:9], v[4:5], 0, v[2:3]
	v_mad_i64_i32 v[4:5], s[26:27], v12, s73, v[6:7]
	v_mul_f32_e32 v152, 0xbfb8aa3b, v152
	v_pk_mul_f32 v[38:39], v[38:39], v[160:161]
	v_lshl_add_u64 v[12:13], v[4:5], 0, v[2:3]
	s_waitcnt vmcnt(4)
	v_mov_b32_e32 v156, v226
	v_mov_b32_e32 v157, v227
	v_mov_b32_e32 v158, v228
	v_mov_b32_e32 v159, v229
	v_lshlrev_b32_e32 v6, 16, v156
	v_and_b32_e32 v7, 0xffff0000, v156
	v_exp_f32_e32 v156, v152
	v_mul_f32_e32 v151, 0xbfb8aa3b, v151
	v_exp_f32_e32 v151, v151
	v_lshlrev_b32_e32 v165, 16, v153
	v_and_b32_e32 v167, 0xffff0000, v153
	v_and_b32_e32 v153, 0xffff0000, v154
	v_lshlrev_b32_e32 v154, 16, v158
	v_add_f32_e32 v11, 1.0, v11
	v_rcp_f32_e32 v152, v11
	v_mul_f32_e32 v11, 0xbfb8aa3b, v154
	v_exp_f32_e32 v154, v11
	v_add_f32_e32 v11, 1.0, v156
	v_rcp_f32_e32 v156, v11
	v_add_f32_e32 v11, 1.0, v151
	v_mul_f32_e32 v151, 0xbfb8aa3b, v153
	v_exp_f32_e32 v151, v151
	v_lshlrev_b32_e32 v168, 16, v155
	v_and_b32_e32 v171, 0xffff0000, v155
	v_and_b32_e32 v155, 0xffff0000, v158
	v_rcp_f32_e32 v153, v11
	v_mul_f32_e32 v11, 0xbfb8aa3b, v155
	v_exp_f32_e32 v155, v11
	v_add_f32_e32 v11, 1.0, v151
	v_mul_f32_e32 v151, 0xbfb8aa3b, v165
	v_exp_f32_e32 v151, v151
	v_lshlrev_b32_e32 v169, 16, v157
	v_and_b32_e32 v172, 0xffff0000, v157
	v_rcp_f32_e32 v157, v11
	v_mul_f32_e32 v11, 0xbfb8aa3b, v169
	v_exp_f32_e32 v158, v11
	v_add_f32_e32 v11, 1.0, v151
	v_mul_f32_e32 v151, 0xbfb8aa3b, v168
	v_exp_f32_e32 v151, v151
	v_lshlrev_b32_e32 v170, 16, v159
	v_rcp_f32_e32 v168, v11
	v_mul_f32_e32 v11, 0xbfb8aa3b, v170
	v_exp_f32_e32 v170, v11
	v_add_f32_e32 v11, 1.0, v151
	v_mul_f32_e32 v151, 0xbfb8aa3b, v167
	v_exp_f32_e32 v151, v151
	v_mul_f32_e32 v6, 0xbfb8aa3b, v6
	v_mul_f32_e32 v7, 0xbfb8aa3b, v7
	v_and_b32_e32 v173, 0xffff0000, v159
	v_exp_f32_e32 v6, v6
	v_exp_f32_e32 v7, v7
	v_mul_f32_e32 v159, 0xbfb8aa3b, v172
	v_rcp_f32_e32 v172, v11
	v_add_f32_e32 v11, 1.0, v151
	v_rcp_f32_e32 v169, v11
	v_mul_f32_e32 v11, 0xbfb8aa3b, v171
	v_exp_f32_e32 v11, v11
	v_pk_add_f32 v[6:7], v[6:7], 1.0 op_sel_hi:[1,0]
	v_exp_f32_e32 v159, v159
	v_pk_mul_f32 v[6:7], v[6:7], v[152:153]
	v_mul_f32_e32 v151, 0xbfb8aa3b, v173
	v_exp_f32_e32 v171, v151
	v_pk_mul_f32 v[30:31], v[30:31], v[6:7]
	v_add_f32_e32 v6, 1.0, v11
	v_rcp_f32_e32 v173, v6
	v_pk_add_f32 v[158:159], v[158:159], 1.0 op_sel_hi:[1,0]
	v_pk_add_f32 v[6:7], v[170:171], 1.0 op_sel_hi:[1,0]
	v_pk_mul_f32 v[152:153], v[158:159], v[168:169]
	s_waitcnt vmcnt(3)
	v_mov_b32_e32 v160, v230
	v_mov_b32_e32 v161, v231
	v_mov_b32_e32 v162, v232
	v_mov_b32_e32 v163, v233
	v_lshlrev_b32_e32 v11, 16, v160
	v_pk_mul_f32 v[32:33], v[32:33], v[152:153]
	v_pk_add_f32 v[152:153], v[154:155], 1.0 op_sel_hi:[1,0]
	v_pk_mul_f32 v[154:155], v[6:7], v[172:173]
	v_pk_mul_f32 v[152:153], v[152:153], v[156:157]
	v_pk_mul_f32 v[36:37], v[36:37], v[154:155]
	v_pk_mul_f32 v[34:35], v[34:35], v[152:153]
	v_lshlrev_b32_e32 v156, 16, v162
	s_waitcnt vmcnt(2)
; __device__ __forceinline__ void unpack8(u32x4 w, f32x4& a, f32x4& b) { a = (f32x4){bflo(w.x), bfhi(w.x), bflo(w.y), bfhi(w.y)}; b = (f32x4){bflo(w.z), bfhi(w.z), bflo(w.w), bfhi(w.w)}; }
;     __device__ __forceinline__ void mid(Acc& acc, const Unit& u, int wr, int wc, int fr, int fq) const {
;         const int row0 = u.row0 + wr * 64 + fr, col0 = u.col0 + wc * 32 + 8 * fq;
; #pragma unroll
;         for (int ai = 0; ai < 2; ++ai)
; #pragma unroll
;             for (int m = 0; m < 4; ++m) { const size_t ro = (size_t)(row0 + ai * HALF + m * 16) * ldg;
; #pragma unroll
;                 for (int bj = 0; bj < 2; ++bj) { const int col = col0 + bj * HALF;
;                     f32x4 a0, a1, b0, b1; unpack8(*(const u32x4*)(GA + ro + col), a0, a1); unpack8(*(const u32x4*)(GB + ro + col), b0, b1);
; #pragma unroll
;                     for (int j = 0; j < 4; ++j) { acc[ai][bj][m][0][j] *= (1.0f + __expf(-b0[j])) * __builtin_amdgcn_rcpf(1.0f + __expf(-a0[j])); acc[ai][bj][m][1][j] *= (1.0f + __expf(-b1[j])) * __builtin_amdgcn_rcpf(1.0f + __expf(-a1[j])); } } }
; template <class Epi, class Sched, bool F8 = false, bool MID = false, bool GATHER = false>
; __device__ __forceinline__ void gemm_phase(LAS unsigned char* lds, const Gemm g, const Sched& S, const Epi& E) {
;     ...
;             if constexpr (MID) { if (t == (nt >> 1)) { if constexpr (F8) asm volatile("s_nop 15\n\ts_nop 15" ::: "memory"); int l_; asm volatile("v_mbcnt_lo_u32_b32 %0, -1, 0\n\tv_mbcnt_hi_u32_b32 %0, -1, %0" : "=v"(l_)); E.mid(acc, cur, wr, wc, l_ & 15, l_ >> 4); if constexpr (F8) asm volatile("s_nop 7" ::: "memory"); } }
	v_mov_b32_e32 v2, v234
	v_mov_b32_e32 v3, v235
	v_mov_b32_e32 v4, v236
	v_mov_b32_e32 v5, v237
	v_lshlrev_b32_e32 v12, 16, v2
	v_and_b32_e32 v158, 0xffff0000, v2
	v_lshlrev_b32_e32 v167, 16, v5
	v_mul_f32_e32 v2, 0xbfb8aa3b, v11
	v_and_b32_e32 v11, 0xffff0000, v5
	v_mul_f32_e32 v5, 0xbfb8aa3b, v156
	v_exp_f32_e32 v5, v5
	v_lshlrev_b32_e32 v157, 16, v161
	v_and_b32_e32 v159, 0xffff0000, v161
	v_and_b32_e32 v13, 0xffff0000, v162
	v_lshlrev_b32_e32 v161, 16, v3
	v_and_b32_e32 v165, 0xffff0000, v3
	v_lshlrev_b32_e32 v3, 16, v4
	v_and_b32_e32 v151, 0xffff0000, v160
	v_mul_f32_e32 v3, 0xbfb8aa3b, v3
	v_mul_f32_e32 v13, 0xbfb8aa3b, v13
	v_and_b32_e32 v162, 0xffff0000, v4
	v_exp_f32_e32 v4, v2
	v_mul_f32_e32 v2, 0xbfb8aa3b, v12
	v_exp_f32_e32 v12, v3
	v_add_f32_e32 v3, 1.0, v5
	v_mul_f32_e32 v5, 0xbfb8aa3b, v151
	v_exp_f32_e32 v151, v13
	v_mul_f32_e32 v157, 0xbfb8aa3b, v157
	v_lshlrev_b32_e32 v160, 16, v163
	v_mul_f32_e32 v13, 0xbfb8aa3b, v162
	v_exp_f32_e32 v162, v157
	v_add_f32_e32 v151, 1.0, v151
	v_mul_f32_e32 v160, 0xbfb8aa3b, v160
	v_rcp_f32_e32 v157, v151
	v_mul_f32_e32 v151, 0xbfb8aa3b, v161
	v_exp_f32_e32 v161, v160
	v_rcp_f32_e32 v156, v3
	v_mul_f32_e32 v3, 0xbfb8aa3b, v158
	v_exp_f32_e32 v158, v151
	v_add_f32_e32 v151, 1.0, v162
	v_rcp_f32_e32 v160, v151
	v_mul_f32_e32 v151, 0xbfb8aa3b, v167
	v_mul_f32_e32 v159, 0xbfb8aa3b, v159
	v_exp_f32_e32 v5, v5
	v_exp_f32_e32 v162, v151
	v_add_f32_e32 v151, 1.0, v161
	v_exp_f32_e32 v161, v159
	v_mul_f32_e32 v159, 0xbfb8aa3b, v165
	v_exp_f32_e32 v2, v2
	v_add_f32_e32 v4, 1.0, v4
	v_exp_f32_e32 v3, v3
	v_add_f32_e32 v5, 1.0, v5
	v_exp_f32_e32 v159, v159
	v_rcp_f32_e32 v168, v151
	v_add_f32_e32 v151, 1.0, v161
	v_rcp_f32_e32 v4, v4
	v_rcp_f32_e32 v5, v5
	v_rcp_f32_e32 v161, v151
	v_pk_add_f32 v[158:159], v[158:159], 1.0 op_sel_hi:[1,0]
	v_pk_add_f32 v[2:3], v[2:3], 1.0 op_sel_hi:[1,0]
	v_and_b32_e32 v163, 0xffff0000, v163
	v_pk_mul_f32 v[2:3], v[2:3], v[4:5]
	v_pk_mul_f32 v[4:5], v[158:159], v[160:161]
	v_pk_mul_f32 v[26:27], v[26:27], v[2:3]
	v_pk_mul_f32 v[28:29], v[28:29], v[4:5]
	v_mul_f32_e32 v4, 0xbfb8aa3b, v163
	v_exp_f32_e32 v4, v4
	v_mul_f32_e32 v5, 0xbfb8aa3b, v11
	v_exp_f32_e32 v163, v5
	v_exp_f32_e32 v13, v13
	v_add_f32_e32 v2, 1.0, v4
	v_rcp_f32_e32 v169, v2
	v_pk_add_f32 v[2:3], v[162:163], 1.0 op_sel_hi:[1,0]
	v_pk_add_f32 v[4:5], v[12:13], 1.0 op_sel_hi:[1,0]
	s_nop 7
	v_pk_mul_f32 v[2:3], v[2:3], v[168:169]
	v_pk_mul_f32 v[4:5], v[4:5], v[156:157]
	v_pk_mul_f32 v[24:25], v[24:25], v[2:3]
	s_waitcnt vmcnt(1)
	v_mov_b32_e32 v6, v238
	v_mov_b32_e32 v7, v239
	v_mov_b32_e32 v8, v240
	v_mov_b32_e32 v9, v241
	v_lshlrev_b32_e32 v2, 16, v6
	v_mul_f32_e32 v2, 0xbfb8aa3b, v2
	v_and_b32_e32 v3, 0xffff0000, v6
	v_lshlrev_b32_e32 v11, 16, v7
	v_and_b32_e32 v13, 0xffff0000, v7
	s_waitcnt vmcnt(0)
	v_mov_b32_e32 v152, v242
	v_mov_b32_e32 v153, v243
	v_mov_b32_e32 v154, v244
	v_mov_b32_e32 v155, v245
	v_lshlrev_b32_e32 v6, 16, v152
	v_and_b32_e32 v7, 0xffff0000, v152
	v_exp_f32_e32 v152, v2
	v_pk_mul_f32 v[22:23], v[22:23], v[4:5]
	v_lshlrev_b32_e32 v4, 16, v8
	v_mul_f32_e32 v4, 0xbfb8aa3b, v4
	v_mul_f32_e32 v2, 0xbfb8aa3b, v6
	v_add_f32_e32 v6, 1.0, v152
	v_exp_f32_e32 v152, v4
	v_and_b32_e32 v5, 0xffff0000, v8
	v_lshlrev_b32_e32 v8, 16, v154
	v_mul_f32_e32 v3, 0xbfb8aa3b, v3
	v_rcp_f32_e32 v4, v6
	v_mul_f32_e32 v6, 0xbfb8aa3b, v8
	v_add_f32_e32 v8, 1.0, v152
	v_exp_f32_e32 v152, v3
	v_mul_f32_e32 v11, 0xbfb8aa3b, v11
	v_lshlrev_b32_e32 v151, 16, v9
	v_mul_f32_e32 v5, 0xbfb8aa3b, v5
	v_exp_f32_e32 v11, v11
	v_mul_f32_e32 v3, 0xbfb8aa3b, v7
	v_add_f32_e32 v7, 1.0, v152
	v_exp_f32_e32 v152, v5
	v_mul_f32_e32 v151, 0xbfb8aa3b, v151
	v_exp_f32_e32 v151, v151
	v_and_b32_e32 v157, 0xffff0000, v9
	v_and_b32_e32 v9, 0xffff0000, v154
	v_lshlrev_b32_e32 v154, 16, v155
	v_add_f32_e32 v11, 1.0, v11
	v_rcp_f32_e32 v5, v7
	v_mul_f32_e32 v7, 0xbfb8aa3b, v9
	v_add_f32_e32 v9, 1.0, v152
	v_rcp_f32_e32 v152, v11
	v_mul_f32_e32 v11, 0xbfb8aa3b, v154
	v_mul_f32_e32 v13, 0xbfb8aa3b, v13
	v_exp_f32_e32 v154, v11
	v_add_f32_e32 v11, 1.0, v151
	v_exp_f32_e32 v151, v13
	v_lshlrev_b32_e32 v12, 16, v153
	v_and_b32_e32 v153, 0xffff0000, v153
	v_mul_f32_e32 v12, 0xbfb8aa3b, v12
	v_mul_f32_e32 v13, 0xbfb8aa3b, v153
	v_exp_f32_e32 v2, v2
	v_exp_f32_e32 v3, v3
	v_exp_f32_e32 v12, v12
	v_exp_f32_e32 v13, v13
	v_rcp_f32_e32 v156, v11
	v_add_f32_e32 v11, 1.0, v151
	v_rcp_f32_e32 v153, v11
	v_pk_add_f32 v[12:13], v[12:13], 1.0 op_sel_hi:[1,0]
	v_pk_add_f32 v[2:3], v[2:3], 1.0 op_sel_hi:[1,0]
	v_and_b32_e32 v155, 0xffff0000, v155
	v_pk_mul_f32 v[2:3], v[2:3], v[4:5]
	v_pk_mul_f32 v[4:5], v[12:13], v[152:153]
	v_exp_f32_e32 v6, v6
	v_pk_mul_f32 v[16:17], v[16:17], v[4:5]
	v_mul_f32_e32 v4, 0xbfb8aa3b, v157
	v_exp_f32_e32 v4, v4
	v_mul_f32_e32 v5, 0xbfb8aa3b, v155
	v_exp_f32_e32 v7, v7
	v_exp_f32_e32 v155, v5
	v_pk_mul_f32 v[14:15], v[14:15], v[2:3]
	v_add_f32_e32 v2, 1.0, v4
	v_rcp_f32_e32 v8, v8
	v_rcp_f32_e32 v9, v9
	v_rcp_f32_e32 v157, v2
	v_pk_add_f32 v[2:3], v[154:155], 1.0 op_sel_hi:[1,0]
	v_pk_add_f32 v[4:5], v[6:7], 1.0 op_sel_hi:[1,0]
	v_pk_mul_f32 v[2:3], v[2:3], v[156:157]
	v_pk_mul_f32 v[4:5], v[4:5], v[8:9]
	v_pk_mul_f32 v[20:21], v[20:21], v[2:3]
	v_pk_mul_f32 v[18:19], v[18:19], v[4:5]
	s_branch .LBB0_1850
